# P0 adaLN GEMV k loop re-emitted: 63 weight-row loads in flight per wave (saddr form), cond rows read 4 ahead
# baseline (speedup 1.0000x reference)
; #define LAS __attribute__((address_space(3)))
; __device__ __forceinline__ void ph0_adaln(const Args& a, LAS unsigned char* lds, int tid, int G, int bid) {
;     ...
;         const int cc = tid & 63, col = ub * 64 + cc, kq = tid >> 6;
;         float acc[8];
; #pragma unroll
;         for (int b = 0; b < 8; ++b) acc[b] = 0.f;
;         const float* wp = W + (size_t)(kq * 256) * MODW + col;
;         for (int k = 0; k < 256; k += 64) {
;             float w[64];
; #pragma unroll
;             for (int q = 0; q < 64; ++q) w[q] = wp[(size_t)(k + q) * MODW];
; #pragma unroll
;             for (int q = 0; q < 64; ++q) { const f32x4 c0 = *(const LAS f32x4*)(cond + (kq * 256 + k + q) * 8), c1 = *(const LAS f32x4*)(cond + (kq * 256 + k + q) * 8 + 4);
.LBB0_32:
	v_ashrrev_i32_e32 v43, 31, v42
	v_mov_b32_e32 v122, 0
	v_lshl_add_u64 v[44:45], v[42:43], 2, v[40:41]
	s_movk_i32 s0, 0xffc0
	v_mov_b32_e32 v43, v148
	v_mov_b32_e32 v123, v122
	v_mov_b32_e32 v124, v122
	v_mov_b32_e32 v125, v122
	v_mov_b32_e32 v126, v122
	v_mov_b32_e32 v127, v122
	v_mov_b32_e32 v128, v122
	v_mov_b32_e32 v129, v122
	v_readfirstlane_b32 s2, v44
	v_readfirstlane_b32 s3, v45
	v_lshlrev_b32_e32 v110, 2, v178
	s_mov_b32 s4, 3
	ds_read_b128 v[2:5], v43 offset:0
	ds_read_b128 v[6:9], v43 offset:16
	ds_read_b128 v[10:13], v43 offset:32
	ds_read_b128 v[14:17], v43 offset:48
	ds_read_b128 v[18:21], v43 offset:64
	ds_read_b128 v[22:25], v43 offset:80
	ds_read_b128 v[26:29], v43 offset:96
	ds_read_b128 v[30:33], v43 offset:112
	global_load_dword v46, v110, s[2:3]
	s_add_u32 s2, s2, 0xc000
	s_addc_u32 s3, s3, 0
	global_load_dword v47, v110, s[2:3]
	s_add_u32 s2, s2, 0xc000
	s_addc_u32 s3, s3, 0
	global_load_dword v48, v110, s[2:3]
	s_add_u32 s2, s2, 0xc000
	s_addc_u32 s3, s3, 0
	global_load_dword v49, v110, s[2:3]
	s_add_u32 s2, s2, 0xc000
	s_addc_u32 s3, s3, 0
	global_load_dword v50, v110, s[2:3]
	s_add_u32 s2, s2, 0xc000
	s_addc_u32 s3, s3, 0
	global_load_dword v51, v110, s[2:3]
	s_add_u32 s2, s2, 0xc000
	s_addc_u32 s3, s3, 0
	global_load_dword v52, v110, s[2:3]
	s_add_u32 s2, s2, 0xc000
	s_addc_u32 s3, s3, 0
	global_load_dword v53, v110, s[2:3]
	s_add_u32 s2, s2, 0xc000
	s_addc_u32 s3, s3, 0
	global_load_dword v54, v110, s[2:3]
	s_add_u32 s2, s2, 0xc000
	s_addc_u32 s3, s3, 0
	global_load_dword v55, v110, s[2:3]
	s_add_u32 s2, s2, 0xc000
	s_addc_u32 s3, s3, 0
	global_load_dword v56, v110, s[2:3]
	s_add_u32 s2, s2, 0xc000
	s_addc_u32 s3, s3, 0
	global_load_dword v57, v110, s[2:3]
	s_add_u32 s2, s2, 0xc000
	s_addc_u32 s3, s3, 0
	global_load_dword v58, v110, s[2:3]
	s_add_u32 s2, s2, 0xc000
	s_addc_u32 s3, s3, 0
	global_load_dword v59, v110, s[2:3]
	s_add_u32 s2, s2, 0xc000
	s_addc_u32 s3, s3, 0
	global_load_dword v60, v110, s[2:3]
	s_add_u32 s2, s2, 0xc000
	s_addc_u32 s3, s3, 0
	global_load_dword v61, v110, s[2:3]
	s_add_u32 s2, s2, 0xc000
	s_addc_u32 s3, s3, 0
	global_load_dword v62, v110, s[2:3]
	s_add_u32 s2, s2, 0xc000
	s_addc_u32 s3, s3, 0
	global_load_dword v63, v110, s[2:3]
	s_add_u32 s2, s2, 0xc000
	s_addc_u32 s3, s3, 0
	global_load_dword v64, v110, s[2:3]
	s_add_u32 s2, s2, 0xc000
	s_addc_u32 s3, s3, 0
	global_load_dword v65, v110, s[2:3]
	s_add_u32 s2, s2, 0xc000
	s_addc_u32 s3, s3, 0
	global_load_dword v66, v110, s[2:3]
	s_add_u32 s2, s2, 0xc000
	s_addc_u32 s3, s3, 0
	global_load_dword v67, v110, s[2:3]
	s_add_u32 s2, s2, 0xc000
	s_addc_u32 s3, s3, 0
	global_load_dword v68, v110, s[2:3]
	s_add_u32 s2, s2, 0xc000
	s_addc_u32 s3, s3, 0
	global_load_dword v69, v110, s[2:3]
	s_add_u32 s2, s2, 0xc000
	s_addc_u32 s3, s3, 0
	global_load_dword v70, v110, s[2:3]
	s_add_u32 s2, s2, 0xc000
	s_addc_u32 s3, s3, 0
	global_load_dword v71, v110, s[2:3]
	s_add_u32 s2, s2, 0xc000
	s_addc_u32 s3, s3, 0
	global_load_dword v72, v110, s[2:3]
	s_add_u32 s2, s2, 0xc000
	s_addc_u32 s3, s3, 0
	global_load_dword v73, v110, s[2:3]
	s_add_u32 s2, s2, 0xc000
	s_addc_u32 s3, s3, 0
	global_load_dword v74, v110, s[2:3]
	s_add_u32 s2, s2, 0xc000
	s_addc_u32 s3, s3, 0
	global_load_dword v75, v110, s[2:3]
	s_add_u32 s2, s2, 0xc000
	s_addc_u32 s3, s3, 0
	global_load_dword v76, v110, s[2:3]
	s_add_u32 s2, s2, 0xc000
	s_addc_u32 s3, s3, 0
	global_load_dword v77, v110, s[2:3]
	s_add_u32 s2, s2, 0xc000
	s_addc_u32 s3, s3, 0
	global_load_dword v78, v110, s[2:3]
	s_add_u32 s2, s2, 0xc000
	s_addc_u32 s3, s3, 0
	global_load_dword v79, v110, s[2:3]
	s_add_u32 s2, s2, 0xc000
	s_addc_u32 s3, s3, 0
	global_load_dword v80, v110, s[2:3]
	s_add_u32 s2, s2, 0xc000
	s_addc_u32 s3, s3, 0
	global_load_dword v81, v110, s[2:3]
	s_add_u32 s2, s2, 0xc000
	s_addc_u32 s3, s3, 0
	global_load_dword v82, v110, s[2:3]
	s_add_u32 s2, s2, 0xc000
	s_addc_u32 s3, s3, 0
	global_load_dword v83, v110, s[2:3]
	s_add_u32 s2, s2, 0xc000
	s_addc_u32 s3, s3, 0
	global_load_dword v84, v110, s[2:3]
	s_add_u32 s2, s2, 0xc000
	s_addc_u32 s3, s3, 0
	global_load_dword v85, v110, s[2:3]
	s_add_u32 s2, s2, 0xc000
	s_addc_u32 s3, s3, 0
	global_load_dword v86, v110, s[2:3]
	s_add_u32 s2, s2, 0xc000
	s_addc_u32 s3, s3, 0
	global_load_dword v87, v110, s[2:3]
	s_add_u32 s2, s2, 0xc000
	s_addc_u32 s3, s3, 0
	global_load_dword v88, v110, s[2:3]
	s_add_u32 s2, s2, 0xc000
	s_addc_u32 s3, s3, 0
	global_load_dword v89, v110, s[2:3]
	s_add_u32 s2, s2, 0xc000
	s_addc_u32 s3, s3, 0
	global_load_dword v90, v110, s[2:3]
	s_add_u32 s2, s2, 0xc000
	s_addc_u32 s3, s3, 0
	global_load_dword v91, v110, s[2:3]
	s_add_u32 s2, s2, 0xc000
	s_addc_u32 s3, s3, 0
	global_load_dword v92, v110, s[2:3]
	s_add_u32 s2, s2, 0xc000
	s_addc_u32 s3, s3, 0
	global_load_dword v93, v110, s[2:3]
	s_add_u32 s2, s2, 0xc000
	s_addc_u32 s3, s3, 0
	global_load_dword v94, v110, s[2:3]
	s_add_u32 s2, s2, 0xc000
	s_addc_u32 s3, s3, 0
	global_load_dword v95, v110, s[2:3]
	s_add_u32 s2, s2, 0xc000
	s_addc_u32 s3, s3, 0
	global_load_dword v96, v110, s[2:3]
	s_add_u32 s2, s2, 0xc000
	s_addc_u32 s3, s3, 0
	global_load_dword v97, v110, s[2:3]
	s_add_u32 s2, s2, 0xc000
	s_addc_u32 s3, s3, 0
	global_load_dword v98, v110, s[2:3]
	s_add_u32 s2, s2, 0xc000
	s_addc_u32 s3, s3, 0
	global_load_dword v99, v110, s[2:3]
	s_add_u32 s2, s2, 0xc000
	s_addc_u32 s3, s3, 0
	global_load_dword v100, v110, s[2:3]
	s_add_u32 s2, s2, 0xc000
	s_addc_u32 s3, s3, 0
	global_load_dword v101, v110, s[2:3]
	s_add_u32 s2, s2, 0xc000
	s_addc_u32 s3, s3, 0
	global_load_dword v102, v110, s[2:3]
	s_add_u32 s2, s2, 0xc000
	s_addc_u32 s3, s3, 0
	global_load_dword v103, v110, s[2:3]
	s_add_u32 s2, s2, 0xc000
	s_addc_u32 s3, s3, 0
	global_load_dword v104, v110, s[2:3]
	s_add_u32 s2, s2, 0xc000
	s_addc_u32 s3, s3, 0
	global_load_dword v105, v110, s[2:3]
	s_add_u32 s2, s2, 0xc000
	s_addc_u32 s3, s3, 0
	global_load_dword v106, v110, s[2:3]
	s_add_u32 s2, s2, 0xc000
	s_addc_u32 s3, s3, 0
	global_load_dword v107, v110, s[2:3]
	s_add_u32 s2, s2, 0xc000
	s_addc_u32 s3, s3, 0
	global_load_dword v108, v110, s[2:3]
	s_add_u32 s2, s2, 0xc000
	s_addc_u32 s3, s3, 0
; #define LAS __attribute__((address_space(3)))
; __device__ __forceinline__ void ph0_adaln(const Args& a, LAS unsigned char* lds, int tid, int G, int bid) {
;     ...
;         for (int k = 0; k < 256; k += 64) {
;             float w[64];
; #pragma unroll
;             for (int q = 0; q < 64; ++q) w[q] = wp[(size_t)(k + q) * MODW];
; #pragma unroll
;             for (int q = 0; q < 64; ++q) { const f32x4 c0 = *(const LAS f32x4*)(cond + (kq * 256 + k + q) * 8), c1 = *(const LAS f32x4*)(cond + (kq * 256 + k + q) * 8 + 4);
;                 acc[0] += w[q] * c0[0]; acc[1] += w[q] * c0[1]; acc[2] += w[q] * c0[2]; acc[3] += w[q] * c0[3];
;                 acc[4] += w[q] * c1[0]; acc[5] += w[q] * c1[1]; acc[6] += w[q] * c1[2]; acc[7] += w[q] * c1[3]; }
.Lada_kloop:
	s_waitcnt vmcnt(62) lgkmcnt(6)
	global_load_dword v109, v110, s[2:3]
	s_add_u32 s2, s2, 0xc000
	s_addc_u32 s3, s3, 0
	v_pk_fma_f32 v[124:125], v[46:47], v[2:3], v[124:125] op_sel_hi:[0,1,1]
	v_pk_fma_f32 v[126:127], v[46:47], v[4:5], v[126:127] op_sel_hi:[0,1,1]
	v_pk_fma_f32 v[128:129], v[46:47], v[6:7], v[128:129] op_sel_hi:[0,1,1]
	v_pk_fma_f32 v[122:123], v[46:47], v[8:9], v[122:123] op_sel_hi:[0,1,1]
	ds_read_b128 v[2:5], v43 offset:128
	ds_read_b128 v[6:9], v43 offset:144
	s_waitcnt vmcnt(62) lgkmcnt(6)
	global_load_dword v46, v110, s[2:3]
	s_add_u32 s2, s2, 0xc000
	s_addc_u32 s3, s3, 0
	v_pk_fma_f32 v[124:125], v[46:47], v[10:11], v[124:125] op_sel:[1,0,0] op_sel_hi:[1,1,1]
	v_pk_fma_f32 v[126:127], v[46:47], v[12:13], v[126:127] op_sel:[1,0,0] op_sel_hi:[1,1,1]
	v_pk_fma_f32 v[128:129], v[46:47], v[14:15], v[128:129] op_sel:[1,0,0] op_sel_hi:[1,1,1]
	v_pk_fma_f32 v[122:123], v[46:47], v[16:17], v[122:123] op_sel:[1,0,0] op_sel_hi:[1,1,1]
	ds_read_b128 v[10:13], v43 offset:160
	ds_read_b128 v[14:17], v43 offset:176
	s_waitcnt vmcnt(62) lgkmcnt(6)
	global_load_dword v47, v110, s[2:3]
	s_add_u32 s2, s2, 0xc000
	s_addc_u32 s3, s3, 0
	v_pk_fma_f32 v[124:125], v[48:49], v[18:19], v[124:125] op_sel_hi:[0,1,1]
	v_pk_fma_f32 v[126:127], v[48:49], v[20:21], v[126:127] op_sel_hi:[0,1,1]
	v_pk_fma_f32 v[128:129], v[48:49], v[22:23], v[128:129] op_sel_hi:[0,1,1]
	v_pk_fma_f32 v[122:123], v[48:49], v[24:25], v[122:123] op_sel_hi:[0,1,1]
	ds_read_b128 v[18:21], v43 offset:192
	ds_read_b128 v[22:25], v43 offset:208
	s_waitcnt vmcnt(62) lgkmcnt(6)
	global_load_dword v48, v110, s[2:3]
	s_add_u32 s2, s2, 0xc000
	s_addc_u32 s3, s3, 0
	v_pk_fma_f32 v[124:125], v[48:49], v[26:27], v[124:125] op_sel:[1,0,0] op_sel_hi:[1,1,1]
	v_pk_fma_f32 v[126:127], v[48:49], v[28:29], v[126:127] op_sel:[1,0,0] op_sel_hi:[1,1,1]
	v_pk_fma_f32 v[128:129], v[48:49], v[30:31], v[128:129] op_sel:[1,0,0] op_sel_hi:[1,1,1]
	v_pk_fma_f32 v[122:123], v[48:49], v[32:33], v[122:123] op_sel:[1,0,0] op_sel_hi:[1,1,1]
	ds_read_b128 v[26:29], v43 offset:224
	ds_read_b128 v[30:33], v43 offset:240
	s_waitcnt vmcnt(62) lgkmcnt(6)
	global_load_dword v49, v110, s[2:3]
	s_add_u32 s2, s2, 0xc000
	s_addc_u32 s3, s3, 0
	v_pk_fma_f32 v[124:125], v[50:51], v[2:3], v[124:125] op_sel_hi:[0,1,1]
	v_pk_fma_f32 v[126:127], v[50:51], v[4:5], v[126:127] op_sel_hi:[0,1,1]
	v_pk_fma_f32 v[128:129], v[50:51], v[6:7], v[128:129] op_sel_hi:[0,1,1]
	v_pk_fma_f32 v[122:123], v[50:51], v[8:9], v[122:123] op_sel_hi:[0,1,1]
	ds_read_b128 v[2:5], v43 offset:256
	ds_read_b128 v[6:9], v43 offset:272
	s_waitcnt vmcnt(62) lgkmcnt(6)
	global_load_dword v50, v110, s[2:3]
	s_add_u32 s2, s2, 0xc000
	s_addc_u32 s3, s3, 0
	v_pk_fma_f32 v[124:125], v[50:51], v[10:11], v[124:125] op_sel:[1,0,0] op_sel_hi:[1,1,1]
	v_pk_fma_f32 v[126:127], v[50:51], v[12:13], v[126:127] op_sel:[1,0,0] op_sel_hi:[1,1,1]
	v_pk_fma_f32 v[128:129], v[50:51], v[14:15], v[128:129] op_sel:[1,0,0] op_sel_hi:[1,1,1]
	v_pk_fma_f32 v[122:123], v[50:51], v[16:17], v[122:123] op_sel:[1,0,0] op_sel_hi:[1,1,1]
	ds_read_b128 v[10:13], v43 offset:288
	ds_read_b128 v[14:17], v43 offset:304
	s_waitcnt vmcnt(62) lgkmcnt(6)
	global_load_dword v51, v110, s[2:3]
	s_add_u32 s2, s2, 0xc000
	s_addc_u32 s3, s3, 0
	v_pk_fma_f32 v[124:125], v[52:53], v[18:19], v[124:125] op_sel_hi:[0,1,1]
	v_pk_fma_f32 v[126:127], v[52:53], v[20:21], v[126:127] op_sel_hi:[0,1,1]
	v_pk_fma_f32 v[128:129], v[52:53], v[22:23], v[128:129] op_sel_hi:[0,1,1]
	v_pk_fma_f32 v[122:123], v[52:53], v[24:25], v[122:123] op_sel_hi:[0,1,1]
	ds_read_b128 v[18:21], v43 offset:320
	ds_read_b128 v[22:25], v43 offset:336
	s_waitcnt vmcnt(62) lgkmcnt(6)
	global_load_dword v52, v110, s[2:3]
	s_add_u32 s2, s2, 0xc000
	s_addc_u32 s3, s3, 0
	v_pk_fma_f32 v[124:125], v[52:53], v[26:27], v[124:125] op_sel:[1,0,0] op_sel_hi:[1,1,1]
	v_pk_fma_f32 v[126:127], v[52:53], v[28:29], v[126:127] op_sel:[1,0,0] op_sel_hi:[1,1,1]
	v_pk_fma_f32 v[128:129], v[52:53], v[30:31], v[128:129] op_sel:[1,0,0] op_sel_hi:[1,1,1]
	v_pk_fma_f32 v[122:123], v[52:53], v[32:33], v[122:123] op_sel:[1,0,0] op_sel_hi:[1,1,1]
	ds_read_b128 v[26:29], v43 offset:352
	ds_read_b128 v[30:33], v43 offset:368
	s_waitcnt vmcnt(62) lgkmcnt(6)
	global_load_dword v53, v110, s[2:3]
	s_add_u32 s2, s2, 0xc000
	s_addc_u32 s3, s3, 0
	v_pk_fma_f32 v[124:125], v[54:55], v[2:3], v[124:125] op_sel_hi:[0,1,1]
	v_pk_fma_f32 v[126:127], v[54:55], v[4:5], v[126:127] op_sel_hi:[0,1,1]
	v_pk_fma_f32 v[128:129], v[54:55], v[6:7], v[128:129] op_sel_hi:[0,1,1]
	v_pk_fma_f32 v[122:123], v[54:55], v[8:9], v[122:123] op_sel_hi:[0,1,1]
	ds_read_b128 v[2:5], v43 offset:384
	ds_read_b128 v[6:9], v43 offset:400
	s_waitcnt vmcnt(62) lgkmcnt(6)
	global_load_dword v54, v110, s[2:3]
	s_add_u32 s2, s2, 0xc000
	s_addc_u32 s3, s3, 0
	v_pk_fma_f32 v[124:125], v[54:55], v[10:11], v[124:125] op_sel:[1,0,0] op_sel_hi:[1,1,1]
	v_pk_fma_f32 v[126:127], v[54:55], v[12:13], v[126:127] op_sel:[1,0,0] op_sel_hi:[1,1,1]
	v_pk_fma_f32 v[128:129], v[54:55], v[14:15], v[128:129] op_sel:[1,0,0] op_sel_hi:[1,1,1]
	v_pk_fma_f32 v[122:123], v[54:55], v[16:17], v[122:123] op_sel:[1,0,0] op_sel_hi:[1,1,1]
	ds_read_b128 v[10:13], v43 offset:416
	ds_read_b128 v[14:17], v43 offset:432
	s_waitcnt vmcnt(62) lgkmcnt(6)
	global_load_dword v55, v110, s[2:3]
	s_add_u32 s2, s2, 0xc000
	s_addc_u32 s3, s3, 0
	v_pk_fma_f32 v[124:125], v[56:57], v[18:19], v[124:125] op_sel_hi:[0,1,1]
	v_pk_fma_f32 v[126:127], v[56:57], v[20:21], v[126:127] op_sel_hi:[0,1,1]
	v_pk_fma_f32 v[128:129], v[56:57], v[22:23], v[128:129] op_sel_hi:[0,1,1]
	v_pk_fma_f32 v[122:123], v[56:57], v[24:25], v[122:123] op_sel_hi:[0,1,1]
	ds_read_b128 v[18:21], v43 offset:448
	ds_read_b128 v[22:25], v43 offset:464
	s_waitcnt vmcnt(62) lgkmcnt(6)
; #define LAS __attribute__((address_space(3)))
; __device__ __forceinline__ void ph0_adaln(const Args& a, LAS unsigned char* lds, int tid, int G, int bid) {
;     ...
;         for (int k = 0; k < 256; k += 64) {
;             float w[64];
; #pragma unroll
;             for (int q = 0; q < 64; ++q) w[q] = wp[(size_t)(k + q) * MODW];
; #pragma unroll
;             for (int q = 0; q < 64; ++q) { const f32x4 c0 = *(const LAS f32x4*)(cond + (kq * 256 + k + q) * 8), c1 = *(const LAS f32x4*)(cond + (kq * 256 + k + q) * 8 + 4);
;                 acc[0] += w[q] * c0[0]; acc[1] += w[q] * c0[1]; acc[2] += w[q] * c0[2]; acc[3] += w[q] * c0[3];
;                 acc[4] += w[q] * c1[0]; acc[5] += w[q] * c1[1]; acc[6] += w[q] * c1[2]; acc[7] += w[q] * c1[3]; }
	global_load_dword v56, v110, s[2:3]
	s_add_u32 s2, s2, 0xc000
	s_addc_u32 s3, s3, 0
	v_pk_fma_f32 v[124:125], v[56:57], v[26:27], v[124:125] op_sel:[1,0,0] op_sel_hi:[1,1,1]
	v_pk_fma_f32 v[126:127], v[56:57], v[28:29], v[126:127] op_sel:[1,0,0] op_sel_hi:[1,1,1]
	v_pk_fma_f32 v[128:129], v[56:57], v[30:31], v[128:129] op_sel:[1,0,0] op_sel_hi:[1,1,1]
	v_pk_fma_f32 v[122:123], v[56:57], v[32:33], v[122:123] op_sel:[1,0,0] op_sel_hi:[1,1,1]
	ds_read_b128 v[26:29], v43 offset:480
	ds_read_b128 v[30:33], v43 offset:496
	s_waitcnt vmcnt(62) lgkmcnt(6)
	global_load_dword v57, v110, s[2:3]
	s_add_u32 s2, s2, 0xc000
	s_addc_u32 s3, s3, 0
	v_pk_fma_f32 v[124:125], v[58:59], v[2:3], v[124:125] op_sel_hi:[0,1,1]
	v_pk_fma_f32 v[126:127], v[58:59], v[4:5], v[126:127] op_sel_hi:[0,1,1]
	v_pk_fma_f32 v[128:129], v[58:59], v[6:7], v[128:129] op_sel_hi:[0,1,1]
	v_pk_fma_f32 v[122:123], v[58:59], v[8:9], v[122:123] op_sel_hi:[0,1,1]
	ds_read_b128 v[2:5], v43 offset:512
	ds_read_b128 v[6:9], v43 offset:528
	s_waitcnt vmcnt(62) lgkmcnt(6)
	global_load_dword v58, v110, s[2:3]
	s_add_u32 s2, s2, 0xc000
	s_addc_u32 s3, s3, 0
	v_pk_fma_f32 v[124:125], v[58:59], v[10:11], v[124:125] op_sel:[1,0,0] op_sel_hi:[1,1,1]
	v_pk_fma_f32 v[126:127], v[58:59], v[12:13], v[126:127] op_sel:[1,0,0] op_sel_hi:[1,1,1]
	v_pk_fma_f32 v[128:129], v[58:59], v[14:15], v[128:129] op_sel:[1,0,0] op_sel_hi:[1,1,1]
	v_pk_fma_f32 v[122:123], v[58:59], v[16:17], v[122:123] op_sel:[1,0,0] op_sel_hi:[1,1,1]
	ds_read_b128 v[10:13], v43 offset:544
	ds_read_b128 v[14:17], v43 offset:560
	s_waitcnt vmcnt(62) lgkmcnt(6)
	global_load_dword v59, v110, s[2:3]
	s_add_u32 s2, s2, 0xc000
	s_addc_u32 s3, s3, 0
	v_pk_fma_f32 v[124:125], v[60:61], v[18:19], v[124:125] op_sel_hi:[0,1,1]
	v_pk_fma_f32 v[126:127], v[60:61], v[20:21], v[126:127] op_sel_hi:[0,1,1]
	v_pk_fma_f32 v[128:129], v[60:61], v[22:23], v[128:129] op_sel_hi:[0,1,1]
	v_pk_fma_f32 v[122:123], v[60:61], v[24:25], v[122:123] op_sel_hi:[0,1,1]
	ds_read_b128 v[18:21], v43 offset:576
	ds_read_b128 v[22:25], v43 offset:592
	s_waitcnt vmcnt(62) lgkmcnt(6)
	global_load_dword v60, v110, s[2:3]
	s_add_u32 s2, s2, 0xc000
	s_addc_u32 s3, s3, 0
	v_pk_fma_f32 v[124:125], v[60:61], v[26:27], v[124:125] op_sel:[1,0,0] op_sel_hi:[1,1,1]
	v_pk_fma_f32 v[126:127], v[60:61], v[28:29], v[126:127] op_sel:[1,0,0] op_sel_hi:[1,1,1]
	v_pk_fma_f32 v[128:129], v[60:61], v[30:31], v[128:129] op_sel:[1,0,0] op_sel_hi:[1,1,1]
	v_pk_fma_f32 v[122:123], v[60:61], v[32:33], v[122:123] op_sel:[1,0,0] op_sel_hi:[1,1,1]
	ds_read_b128 v[26:29], v43 offset:608
	ds_read_b128 v[30:33], v43 offset:624
	s_waitcnt vmcnt(62) lgkmcnt(6)
	global_load_dword v61, v110, s[2:3]
	s_add_u32 s2, s2, 0xc000
	s_addc_u32 s3, s3, 0
	v_pk_fma_f32 v[124:125], v[62:63], v[2:3], v[124:125] op_sel_hi:[0,1,1]
	v_pk_fma_f32 v[126:127], v[62:63], v[4:5], v[126:127] op_sel_hi:[0,1,1]
	v_pk_fma_f32 v[128:129], v[62:63], v[6:7], v[128:129] op_sel_hi:[0,1,1]
	v_pk_fma_f32 v[122:123], v[62:63], v[8:9], v[122:123] op_sel_hi:[0,1,1]
	ds_read_b128 v[2:5], v43 offset:640
	ds_read_b128 v[6:9], v43 offset:656
	s_waitcnt vmcnt(62) lgkmcnt(6)
	global_load_dword v62, v110, s[2:3]
	s_add_u32 s2, s2, 0xc000
	s_addc_u32 s3, s3, 0
	v_pk_fma_f32 v[124:125], v[62:63], v[10:11], v[124:125] op_sel:[1,0,0] op_sel_hi:[1,1,1]
	v_pk_fma_f32 v[126:127], v[62:63], v[12:13], v[126:127] op_sel:[1,0,0] op_sel_hi:[1,1,1]
	v_pk_fma_f32 v[128:129], v[62:63], v[14:15], v[128:129] op_sel:[1,0,0] op_sel_hi:[1,1,1]
	v_pk_fma_f32 v[122:123], v[62:63], v[16:17], v[122:123] op_sel:[1,0,0] op_sel_hi:[1,1,1]
	ds_read_b128 v[10:13], v43 offset:672
	ds_read_b128 v[14:17], v43 offset:688
	s_waitcnt vmcnt(62) lgkmcnt(6)
	global_load_dword v63, v110, s[2:3]
	s_add_u32 s2, s2, 0xc000
	s_addc_u32 s3, s3, 0
	v_pk_fma_f32 v[124:125], v[64:65], v[18:19], v[124:125] op_sel_hi:[0,1,1]
	v_pk_fma_f32 v[126:127], v[64:65], v[20:21], v[126:127] op_sel_hi:[0,1,1]
	v_pk_fma_f32 v[128:129], v[64:65], v[22:23], v[128:129] op_sel_hi:[0,1,1]
	v_pk_fma_f32 v[122:123], v[64:65], v[24:25], v[122:123] op_sel_hi:[0,1,1]
	ds_read_b128 v[18:21], v43 offset:704
	ds_read_b128 v[22:25], v43 offset:720
	s_waitcnt vmcnt(62) lgkmcnt(6)
	global_load_dword v64, v110, s[2:3]
	s_add_u32 s2, s2, 0xc000
	s_addc_u32 s3, s3, 0
	v_pk_fma_f32 v[124:125], v[64:65], v[26:27], v[124:125] op_sel:[1,0,0] op_sel_hi:[1,1,1]
	v_pk_fma_f32 v[126:127], v[64:65], v[28:29], v[126:127] op_sel:[1,0,0] op_sel_hi:[1,1,1]
	v_pk_fma_f32 v[128:129], v[64:65], v[30:31], v[128:129] op_sel:[1,0,0] op_sel_hi:[1,1,1]
	v_pk_fma_f32 v[122:123], v[64:65], v[32:33], v[122:123] op_sel:[1,0,0] op_sel_hi:[1,1,1]
	ds_read_b128 v[26:29], v43 offset:736
	ds_read_b128 v[30:33], v43 offset:752
	s_waitcnt vmcnt(62) lgkmcnt(6)
	global_load_dword v65, v110, s[2:3]
	s_add_u32 s2, s2, 0xc000
	s_addc_u32 s3, s3, 0
	v_pk_fma_f32 v[124:125], v[66:67], v[2:3], v[124:125] op_sel_hi:[0,1,1]
	v_pk_fma_f32 v[126:127], v[66:67], v[4:5], v[126:127] op_sel_hi:[0,1,1]
	v_pk_fma_f32 v[128:129], v[66:67], v[6:7], v[128:129] op_sel_hi:[0,1,1]
	v_pk_fma_f32 v[122:123], v[66:67], v[8:9], v[122:123] op_sel_hi:[0,1,1]
	ds_read_b128 v[2:5], v43 offset:768
	ds_read_b128 v[6:9], v43 offset:784
	s_waitcnt vmcnt(62) lgkmcnt(6)
	global_load_dword v66, v110, s[2:3]
	s_add_u32 s2, s2, 0xc000
	s_addc_u32 s3, s3, 0
	v_pk_fma_f32 v[124:125], v[66:67], v[10:11], v[124:125] op_sel:[1,0,0] op_sel_hi:[1,1,1]
	v_pk_fma_f32 v[126:127], v[66:67], v[12:13], v[126:127] op_sel:[1,0,0] op_sel_hi:[1,1,1]
	v_pk_fma_f32 v[128:129], v[66:67], v[14:15], v[128:129] op_sel:[1,0,0] op_sel_hi:[1,1,1]
	v_pk_fma_f32 v[122:123], v[66:67], v[16:17], v[122:123] op_sel:[1,0,0] op_sel_hi:[1,1,1]
	ds_read_b128 v[10:13], v43 offset:800
	ds_read_b128 v[14:17], v43 offset:816
	s_waitcnt vmcnt(62) lgkmcnt(6)
; #define LAS __attribute__((address_space(3)))
; __device__ __forceinline__ void ph0_adaln(const Args& a, LAS unsigned char* lds, int tid, int G, int bid) {
;     ...
;         for (int k = 0; k < 256; k += 64) {
;             float w[64];
; #pragma unroll
;             for (int q = 0; q < 64; ++q) w[q] = wp[(size_t)(k + q) * MODW];
; #pragma unroll
;             for (int q = 0; q < 64; ++q) { const f32x4 c0 = *(const LAS f32x4*)(cond + (kq * 256 + k + q) * 8), c1 = *(const LAS f32x4*)(cond + (kq * 256 + k + q) * 8 + 4);
;                 acc[0] += w[q] * c0[0]; acc[1] += w[q] * c0[1]; acc[2] += w[q] * c0[2]; acc[3] += w[q] * c0[3];
;                 acc[4] += w[q] * c1[0]; acc[5] += w[q] * c1[1]; acc[6] += w[q] * c1[2]; acc[7] += w[q] * c1[3]; }
	global_load_dword v67, v110, s[2:3]
	s_add_u32 s2, s2, 0xc000
	s_addc_u32 s3, s3, 0
	v_pk_fma_f32 v[124:125], v[68:69], v[18:19], v[124:125] op_sel_hi:[0,1,1]
	v_pk_fma_f32 v[126:127], v[68:69], v[20:21], v[126:127] op_sel_hi:[0,1,1]
	v_pk_fma_f32 v[128:129], v[68:69], v[22:23], v[128:129] op_sel_hi:[0,1,1]
	v_pk_fma_f32 v[122:123], v[68:69], v[24:25], v[122:123] op_sel_hi:[0,1,1]
	ds_read_b128 v[18:21], v43 offset:832
	ds_read_b128 v[22:25], v43 offset:848
	s_waitcnt vmcnt(62) lgkmcnt(6)
	global_load_dword v68, v110, s[2:3]
	s_add_u32 s2, s2, 0xc000
	s_addc_u32 s3, s3, 0
	v_pk_fma_f32 v[124:125], v[68:69], v[26:27], v[124:125] op_sel:[1,0,0] op_sel_hi:[1,1,1]
	v_pk_fma_f32 v[126:127], v[68:69], v[28:29], v[126:127] op_sel:[1,0,0] op_sel_hi:[1,1,1]
	v_pk_fma_f32 v[128:129], v[68:69], v[30:31], v[128:129] op_sel:[1,0,0] op_sel_hi:[1,1,1]
	v_pk_fma_f32 v[122:123], v[68:69], v[32:33], v[122:123] op_sel:[1,0,0] op_sel_hi:[1,1,1]
	ds_read_b128 v[26:29], v43 offset:864
	ds_read_b128 v[30:33], v43 offset:880
	s_waitcnt vmcnt(62) lgkmcnt(6)
	global_load_dword v69, v110, s[2:3]
	s_add_u32 s2, s2, 0xc000
	s_addc_u32 s3, s3, 0
	v_pk_fma_f32 v[124:125], v[70:71], v[2:3], v[124:125] op_sel_hi:[0,1,1]
	v_pk_fma_f32 v[126:127], v[70:71], v[4:5], v[126:127] op_sel_hi:[0,1,1]
	v_pk_fma_f32 v[128:129], v[70:71], v[6:7], v[128:129] op_sel_hi:[0,1,1]
	v_pk_fma_f32 v[122:123], v[70:71], v[8:9], v[122:123] op_sel_hi:[0,1,1]
	ds_read_b128 v[2:5], v43 offset:896
	ds_read_b128 v[6:9], v43 offset:912
	s_waitcnt vmcnt(62) lgkmcnt(6)
	global_load_dword v70, v110, s[2:3]
	s_add_u32 s2, s2, 0xc000
	s_addc_u32 s3, s3, 0
	v_pk_fma_f32 v[124:125], v[70:71], v[10:11], v[124:125] op_sel:[1,0,0] op_sel_hi:[1,1,1]
	v_pk_fma_f32 v[126:127], v[70:71], v[12:13], v[126:127] op_sel:[1,0,0] op_sel_hi:[1,1,1]
	v_pk_fma_f32 v[128:129], v[70:71], v[14:15], v[128:129] op_sel:[1,0,0] op_sel_hi:[1,1,1]
	v_pk_fma_f32 v[122:123], v[70:71], v[16:17], v[122:123] op_sel:[1,0,0] op_sel_hi:[1,1,1]
	ds_read_b128 v[10:13], v43 offset:928
	ds_read_b128 v[14:17], v43 offset:944
	s_waitcnt vmcnt(62) lgkmcnt(6)
	global_load_dword v71, v110, s[2:3]
	s_add_u32 s2, s2, 0xc000
	s_addc_u32 s3, s3, 0
	v_pk_fma_f32 v[124:125], v[72:73], v[18:19], v[124:125] op_sel_hi:[0,1,1]
	v_pk_fma_f32 v[126:127], v[72:73], v[20:21], v[126:127] op_sel_hi:[0,1,1]
	v_pk_fma_f32 v[128:129], v[72:73], v[22:23], v[128:129] op_sel_hi:[0,1,1]
	v_pk_fma_f32 v[122:123], v[72:73], v[24:25], v[122:123] op_sel_hi:[0,1,1]
	ds_read_b128 v[18:21], v43 offset:960
	ds_read_b128 v[22:25], v43 offset:976
	s_waitcnt vmcnt(62) lgkmcnt(6)
	global_load_dword v72, v110, s[2:3]
	s_add_u32 s2, s2, 0xc000
	s_addc_u32 s3, s3, 0
	v_pk_fma_f32 v[124:125], v[72:73], v[26:27], v[124:125] op_sel:[1,0,0] op_sel_hi:[1,1,1]
	v_pk_fma_f32 v[126:127], v[72:73], v[28:29], v[126:127] op_sel:[1,0,0] op_sel_hi:[1,1,1]
	v_pk_fma_f32 v[128:129], v[72:73], v[30:31], v[128:129] op_sel:[1,0,0] op_sel_hi:[1,1,1]
	v_pk_fma_f32 v[122:123], v[72:73], v[32:33], v[122:123] op_sel:[1,0,0] op_sel_hi:[1,1,1]
	ds_read_b128 v[26:29], v43 offset:992
	ds_read_b128 v[30:33], v43 offset:1008
	s_waitcnt vmcnt(62) lgkmcnt(6)
	global_load_dword v73, v110, s[2:3]
	s_add_u32 s2, s2, 0xc000
	s_addc_u32 s3, s3, 0
	v_pk_fma_f32 v[124:125], v[74:75], v[2:3], v[124:125] op_sel_hi:[0,1,1]
	v_pk_fma_f32 v[126:127], v[74:75], v[4:5], v[126:127] op_sel_hi:[0,1,1]
	v_pk_fma_f32 v[128:129], v[74:75], v[6:7], v[128:129] op_sel_hi:[0,1,1]
	v_pk_fma_f32 v[122:123], v[74:75], v[8:9], v[122:123] op_sel_hi:[0,1,1]
	ds_read_b128 v[2:5], v43 offset:1024
	ds_read_b128 v[6:9], v43 offset:1040
	s_waitcnt vmcnt(62) lgkmcnt(6)
	global_load_dword v74, v110, s[2:3]
	s_add_u32 s2, s2, 0xc000
	s_addc_u32 s3, s3, 0
	v_pk_fma_f32 v[124:125], v[74:75], v[10:11], v[124:125] op_sel:[1,0,0] op_sel_hi:[1,1,1]
	v_pk_fma_f32 v[126:127], v[74:75], v[12:13], v[126:127] op_sel:[1,0,0] op_sel_hi:[1,1,1]
	v_pk_fma_f32 v[128:129], v[74:75], v[14:15], v[128:129] op_sel:[1,0,0] op_sel_hi:[1,1,1]
	v_pk_fma_f32 v[122:123], v[74:75], v[16:17], v[122:123] op_sel:[1,0,0] op_sel_hi:[1,1,1]
	ds_read_b128 v[10:13], v43 offset:1056
	ds_read_b128 v[14:17], v43 offset:1072
	s_waitcnt vmcnt(62) lgkmcnt(6)
	global_load_dword v75, v110, s[2:3]
	s_add_u32 s2, s2, 0xc000
	s_addc_u32 s3, s3, 0
	v_pk_fma_f32 v[124:125], v[76:77], v[18:19], v[124:125] op_sel_hi:[0,1,1]
	v_pk_fma_f32 v[126:127], v[76:77], v[20:21], v[126:127] op_sel_hi:[0,1,1]
	v_pk_fma_f32 v[128:129], v[76:77], v[22:23], v[128:129] op_sel_hi:[0,1,1]
	v_pk_fma_f32 v[122:123], v[76:77], v[24:25], v[122:123] op_sel_hi:[0,1,1]
	ds_read_b128 v[18:21], v43 offset:1088
	ds_read_b128 v[22:25], v43 offset:1104
	s_waitcnt vmcnt(62) lgkmcnt(6)
	global_load_dword v76, v110, s[2:3]
	s_add_u32 s2, s2, 0xc000
	s_addc_u32 s3, s3, 0
	v_pk_fma_f32 v[124:125], v[76:77], v[26:27], v[124:125] op_sel:[1,0,0] op_sel_hi:[1,1,1]
	v_pk_fma_f32 v[126:127], v[76:77], v[28:29], v[126:127] op_sel:[1,0,0] op_sel_hi:[1,1,1]
	v_pk_fma_f32 v[128:129], v[76:77], v[30:31], v[128:129] op_sel:[1,0,0] op_sel_hi:[1,1,1]
	v_pk_fma_f32 v[122:123], v[76:77], v[32:33], v[122:123] op_sel:[1,0,0] op_sel_hi:[1,1,1]
	ds_read_b128 v[26:29], v43 offset:1120
	ds_read_b128 v[30:33], v43 offset:1136
	s_waitcnt vmcnt(62) lgkmcnt(6)
	global_load_dword v77, v110, s[2:3]
	s_add_u32 s2, s2, 0xc000
	s_addc_u32 s3, s3, 0
	v_pk_fma_f32 v[124:125], v[78:79], v[2:3], v[124:125] op_sel_hi:[0,1,1]
	v_pk_fma_f32 v[126:127], v[78:79], v[4:5], v[126:127] op_sel_hi:[0,1,1]
	v_pk_fma_f32 v[128:129], v[78:79], v[6:7], v[128:129] op_sel_hi:[0,1,1]
	v_pk_fma_f32 v[122:123], v[78:79], v[8:9], v[122:123] op_sel_hi:[0,1,1]
	ds_read_b128 v[2:5], v43 offset:1152
	ds_read_b128 v[6:9], v43 offset:1168
	s_waitcnt vmcnt(62) lgkmcnt(6)
; #define LAS __attribute__((address_space(3)))
; __device__ __forceinline__ void ph0_adaln(const Args& a, LAS unsigned char* lds, int tid, int G, int bid) {
;     ...
;         for (int k = 0; k < 256; k += 64) {
;             float w[64];
; #pragma unroll
;             for (int q = 0; q < 64; ++q) w[q] = wp[(size_t)(k + q) * MODW];
; #pragma unroll
;             for (int q = 0; q < 64; ++q) { const f32x4 c0 = *(const LAS f32x4*)(cond + (kq * 256 + k + q) * 8), c1 = *(const LAS f32x4*)(cond + (kq * 256 + k + q) * 8 + 4);
;                 acc[0] += w[q] * c0[0]; acc[1] += w[q] * c0[1]; acc[2] += w[q] * c0[2]; acc[3] += w[q] * c0[3];
;                 acc[4] += w[q] * c1[0]; acc[5] += w[q] * c1[1]; acc[6] += w[q] * c1[2]; acc[7] += w[q] * c1[3]; }
	global_load_dword v78, v110, s[2:3]
	s_add_u32 s2, s2, 0xc000
	s_addc_u32 s3, s3, 0
	v_pk_fma_f32 v[124:125], v[78:79], v[10:11], v[124:125] op_sel:[1,0,0] op_sel_hi:[1,1,1]
	v_pk_fma_f32 v[126:127], v[78:79], v[12:13], v[126:127] op_sel:[1,0,0] op_sel_hi:[1,1,1]
	v_pk_fma_f32 v[128:129], v[78:79], v[14:15], v[128:129] op_sel:[1,0,0] op_sel_hi:[1,1,1]
	v_pk_fma_f32 v[122:123], v[78:79], v[16:17], v[122:123] op_sel:[1,0,0] op_sel_hi:[1,1,1]
	ds_read_b128 v[10:13], v43 offset:1184
	ds_read_b128 v[14:17], v43 offset:1200
	s_waitcnt vmcnt(62) lgkmcnt(6)
	global_load_dword v79, v110, s[2:3]
	s_add_u32 s2, s2, 0xc000
	s_addc_u32 s3, s3, 0
	v_pk_fma_f32 v[124:125], v[80:81], v[18:19], v[124:125] op_sel_hi:[0,1,1]
	v_pk_fma_f32 v[126:127], v[80:81], v[20:21], v[126:127] op_sel_hi:[0,1,1]
	v_pk_fma_f32 v[128:129], v[80:81], v[22:23], v[128:129] op_sel_hi:[0,1,1]
	v_pk_fma_f32 v[122:123], v[80:81], v[24:25], v[122:123] op_sel_hi:[0,1,1]
	ds_read_b128 v[18:21], v43 offset:1216
	ds_read_b128 v[22:25], v43 offset:1232
	s_waitcnt vmcnt(62) lgkmcnt(6)
	global_load_dword v80, v110, s[2:3]
	s_add_u32 s2, s2, 0xc000
	s_addc_u32 s3, s3, 0
	v_pk_fma_f32 v[124:125], v[80:81], v[26:27], v[124:125] op_sel:[1,0,0] op_sel_hi:[1,1,1]
	v_pk_fma_f32 v[126:127], v[80:81], v[28:29], v[126:127] op_sel:[1,0,0] op_sel_hi:[1,1,1]
	v_pk_fma_f32 v[128:129], v[80:81], v[30:31], v[128:129] op_sel:[1,0,0] op_sel_hi:[1,1,1]
	v_pk_fma_f32 v[122:123], v[80:81], v[32:33], v[122:123] op_sel:[1,0,0] op_sel_hi:[1,1,1]
	ds_read_b128 v[26:29], v43 offset:1248
	ds_read_b128 v[30:33], v43 offset:1264
	s_waitcnt vmcnt(62) lgkmcnt(6)
	global_load_dword v81, v110, s[2:3]
	s_add_u32 s2, s2, 0xc000
	s_addc_u32 s3, s3, 0
	v_pk_fma_f32 v[124:125], v[82:83], v[2:3], v[124:125] op_sel_hi:[0,1,1]
	v_pk_fma_f32 v[126:127], v[82:83], v[4:5], v[126:127] op_sel_hi:[0,1,1]
	v_pk_fma_f32 v[128:129], v[82:83], v[6:7], v[128:129] op_sel_hi:[0,1,1]
	v_pk_fma_f32 v[122:123], v[82:83], v[8:9], v[122:123] op_sel_hi:[0,1,1]
	ds_read_b128 v[2:5], v43 offset:1280
	ds_read_b128 v[6:9], v43 offset:1296
	s_waitcnt vmcnt(62) lgkmcnt(6)
	global_load_dword v82, v110, s[2:3]
	s_add_u32 s2, s2, 0xc000
	s_addc_u32 s3, s3, 0
	v_pk_fma_f32 v[124:125], v[82:83], v[10:11], v[124:125] op_sel:[1,0,0] op_sel_hi:[1,1,1]
	v_pk_fma_f32 v[126:127], v[82:83], v[12:13], v[126:127] op_sel:[1,0,0] op_sel_hi:[1,1,1]
	v_pk_fma_f32 v[128:129], v[82:83], v[14:15], v[128:129] op_sel:[1,0,0] op_sel_hi:[1,1,1]
	v_pk_fma_f32 v[122:123], v[82:83], v[16:17], v[122:123] op_sel:[1,0,0] op_sel_hi:[1,1,1]
	ds_read_b128 v[10:13], v43 offset:1312
	ds_read_b128 v[14:17], v43 offset:1328
	s_waitcnt vmcnt(62) lgkmcnt(6)
	global_load_dword v83, v110, s[2:3]
	s_add_u32 s2, s2, 0xc000
	s_addc_u32 s3, s3, 0
	v_pk_fma_f32 v[124:125], v[84:85], v[18:19], v[124:125] op_sel_hi:[0,1,1]
	v_pk_fma_f32 v[126:127], v[84:85], v[20:21], v[126:127] op_sel_hi:[0,1,1]
	v_pk_fma_f32 v[128:129], v[84:85], v[22:23], v[128:129] op_sel_hi:[0,1,1]
	v_pk_fma_f32 v[122:123], v[84:85], v[24:25], v[122:123] op_sel_hi:[0,1,1]
	ds_read_b128 v[18:21], v43 offset:1344
	ds_read_b128 v[22:25], v43 offset:1360
	s_waitcnt vmcnt(62) lgkmcnt(6)
	global_load_dword v84, v110, s[2:3]
	s_add_u32 s2, s2, 0xc000
	s_addc_u32 s3, s3, 0
	v_pk_fma_f32 v[124:125], v[84:85], v[26:27], v[124:125] op_sel:[1,0,0] op_sel_hi:[1,1,1]
	v_pk_fma_f32 v[126:127], v[84:85], v[28:29], v[126:127] op_sel:[1,0,0] op_sel_hi:[1,1,1]
	v_pk_fma_f32 v[128:129], v[84:85], v[30:31], v[128:129] op_sel:[1,0,0] op_sel_hi:[1,1,1]
	v_pk_fma_f32 v[122:123], v[84:85], v[32:33], v[122:123] op_sel:[1,0,0] op_sel_hi:[1,1,1]
	ds_read_b128 v[26:29], v43 offset:1376
	ds_read_b128 v[30:33], v43 offset:1392
	s_waitcnt vmcnt(62) lgkmcnt(6)
	global_load_dword v85, v110, s[2:3]
	s_add_u32 s2, s2, 0xc000
	s_addc_u32 s3, s3, 0
	v_pk_fma_f32 v[124:125], v[86:87], v[2:3], v[124:125] op_sel_hi:[0,1,1]
	v_pk_fma_f32 v[126:127], v[86:87], v[4:5], v[126:127] op_sel_hi:[0,1,1]
	v_pk_fma_f32 v[128:129], v[86:87], v[6:7], v[128:129] op_sel_hi:[0,1,1]
	v_pk_fma_f32 v[122:123], v[86:87], v[8:9], v[122:123] op_sel_hi:[0,1,1]
	ds_read_b128 v[2:5], v43 offset:1408
	ds_read_b128 v[6:9], v43 offset:1424
	s_waitcnt vmcnt(62) lgkmcnt(6)
	global_load_dword v86, v110, s[2:3]
	s_add_u32 s2, s2, 0xc000
	s_addc_u32 s3, s3, 0
	v_pk_fma_f32 v[124:125], v[86:87], v[10:11], v[124:125] op_sel:[1,0,0] op_sel_hi:[1,1,1]
	v_pk_fma_f32 v[126:127], v[86:87], v[12:13], v[126:127] op_sel:[1,0,0] op_sel_hi:[1,1,1]
	v_pk_fma_f32 v[128:129], v[86:87], v[14:15], v[128:129] op_sel:[1,0,0] op_sel_hi:[1,1,1]
	v_pk_fma_f32 v[122:123], v[86:87], v[16:17], v[122:123] op_sel:[1,0,0] op_sel_hi:[1,1,1]
	ds_read_b128 v[10:13], v43 offset:1440
	ds_read_b128 v[14:17], v43 offset:1456
	s_waitcnt vmcnt(62) lgkmcnt(6)
	global_load_dword v87, v110, s[2:3]
	s_add_u32 s2, s2, 0xc000
	s_addc_u32 s3, s3, 0
	v_pk_fma_f32 v[124:125], v[88:89], v[18:19], v[124:125] op_sel_hi:[0,1,1]
	v_pk_fma_f32 v[126:127], v[88:89], v[20:21], v[126:127] op_sel_hi:[0,1,1]
	v_pk_fma_f32 v[128:129], v[88:89], v[22:23], v[128:129] op_sel_hi:[0,1,1]
	v_pk_fma_f32 v[122:123], v[88:89], v[24:25], v[122:123] op_sel_hi:[0,1,1]
	ds_read_b128 v[18:21], v43 offset:1472
	ds_read_b128 v[22:25], v43 offset:1488
	s_waitcnt vmcnt(62) lgkmcnt(6)
	global_load_dword v88, v110, s[2:3]
	s_add_u32 s2, s2, 0xc000
	s_addc_u32 s3, s3, 0
	v_pk_fma_f32 v[124:125], v[88:89], v[26:27], v[124:125] op_sel:[1,0,0] op_sel_hi:[1,1,1]
	v_pk_fma_f32 v[126:127], v[88:89], v[28:29], v[126:127] op_sel:[1,0,0] op_sel_hi:[1,1,1]
	v_pk_fma_f32 v[128:129], v[88:89], v[30:31], v[128:129] op_sel:[1,0,0] op_sel_hi:[1,1,1]
	v_pk_fma_f32 v[122:123], v[88:89], v[32:33], v[122:123] op_sel:[1,0,0] op_sel_hi:[1,1,1]
	ds_read_b128 v[26:29], v43 offset:1504
	ds_read_b128 v[30:33], v43 offset:1520
	s_waitcnt vmcnt(62) lgkmcnt(6)
; #define LAS __attribute__((address_space(3)))
; __device__ __forceinline__ void ph0_adaln(const Args& a, LAS unsigned char* lds, int tid, int G, int bid) {
;     ...
;         for (int k = 0; k < 256; k += 64) {
;             float w[64];
; #pragma unroll
;             for (int q = 0; q < 64; ++q) w[q] = wp[(size_t)(k + q) * MODW];
; #pragma unroll
;             for (int q = 0; q < 64; ++q) { const f32x4 c0 = *(const LAS f32x4*)(cond + (kq * 256 + k + q) * 8), c1 = *(const LAS f32x4*)(cond + (kq * 256 + k + q) * 8 + 4);
;                 acc[0] += w[q] * c0[0]; acc[1] += w[q] * c0[1]; acc[2] += w[q] * c0[2]; acc[3] += w[q] * c0[3];
;                 acc[4] += w[q] * c1[0]; acc[5] += w[q] * c1[1]; acc[6] += w[q] * c1[2]; acc[7] += w[q] * c1[3]; }
	global_load_dword v89, v110, s[2:3]
	s_add_u32 s2, s2, 0xc000
	s_addc_u32 s3, s3, 0
	v_pk_fma_f32 v[124:125], v[90:91], v[2:3], v[124:125] op_sel_hi:[0,1,1]
	v_pk_fma_f32 v[126:127], v[90:91], v[4:5], v[126:127] op_sel_hi:[0,1,1]
	v_pk_fma_f32 v[128:129], v[90:91], v[6:7], v[128:129] op_sel_hi:[0,1,1]
	v_pk_fma_f32 v[122:123], v[90:91], v[8:9], v[122:123] op_sel_hi:[0,1,1]
	ds_read_b128 v[2:5], v43 offset:1536
	ds_read_b128 v[6:9], v43 offset:1552
	s_waitcnt vmcnt(62) lgkmcnt(6)
	global_load_dword v90, v110, s[2:3]
	s_add_u32 s2, s2, 0xc000
	s_addc_u32 s3, s3, 0
	v_pk_fma_f32 v[124:125], v[90:91], v[10:11], v[124:125] op_sel:[1,0,0] op_sel_hi:[1,1,1]
	v_pk_fma_f32 v[126:127], v[90:91], v[12:13], v[126:127] op_sel:[1,0,0] op_sel_hi:[1,1,1]
	v_pk_fma_f32 v[128:129], v[90:91], v[14:15], v[128:129] op_sel:[1,0,0] op_sel_hi:[1,1,1]
	v_pk_fma_f32 v[122:123], v[90:91], v[16:17], v[122:123] op_sel:[1,0,0] op_sel_hi:[1,1,1]
	ds_read_b128 v[10:13], v43 offset:1568
	ds_read_b128 v[14:17], v43 offset:1584
	s_waitcnt vmcnt(62) lgkmcnt(6)
	global_load_dword v91, v110, s[2:3]
	s_add_u32 s2, s2, 0xc000
	s_addc_u32 s3, s3, 0
	v_pk_fma_f32 v[124:125], v[92:93], v[18:19], v[124:125] op_sel_hi:[0,1,1]
	v_pk_fma_f32 v[126:127], v[92:93], v[20:21], v[126:127] op_sel_hi:[0,1,1]
	v_pk_fma_f32 v[128:129], v[92:93], v[22:23], v[128:129] op_sel_hi:[0,1,1]
	v_pk_fma_f32 v[122:123], v[92:93], v[24:25], v[122:123] op_sel_hi:[0,1,1]
	ds_read_b128 v[18:21], v43 offset:1600
	ds_read_b128 v[22:25], v43 offset:1616
	s_waitcnt vmcnt(62) lgkmcnt(6)
	global_load_dword v92, v110, s[2:3]
	s_add_u32 s2, s2, 0xc000
	s_addc_u32 s3, s3, 0
	v_pk_fma_f32 v[124:125], v[92:93], v[26:27], v[124:125] op_sel:[1,0,0] op_sel_hi:[1,1,1]
	v_pk_fma_f32 v[126:127], v[92:93], v[28:29], v[126:127] op_sel:[1,0,0] op_sel_hi:[1,1,1]
	v_pk_fma_f32 v[128:129], v[92:93], v[30:31], v[128:129] op_sel:[1,0,0] op_sel_hi:[1,1,1]
	v_pk_fma_f32 v[122:123], v[92:93], v[32:33], v[122:123] op_sel:[1,0,0] op_sel_hi:[1,1,1]
	ds_read_b128 v[26:29], v43 offset:1632
	ds_read_b128 v[30:33], v43 offset:1648
	s_waitcnt vmcnt(62) lgkmcnt(6)
	global_load_dword v93, v110, s[2:3]
	s_add_u32 s2, s2, 0xc000
	s_addc_u32 s3, s3, 0
	v_pk_fma_f32 v[124:125], v[94:95], v[2:3], v[124:125] op_sel_hi:[0,1,1]
	v_pk_fma_f32 v[126:127], v[94:95], v[4:5], v[126:127] op_sel_hi:[0,1,1]
	v_pk_fma_f32 v[128:129], v[94:95], v[6:7], v[128:129] op_sel_hi:[0,1,1]
	v_pk_fma_f32 v[122:123], v[94:95], v[8:9], v[122:123] op_sel_hi:[0,1,1]
	ds_read_b128 v[2:5], v43 offset:1664
	ds_read_b128 v[6:9], v43 offset:1680
	s_waitcnt vmcnt(62) lgkmcnt(6)
	global_load_dword v94, v110, s[2:3]
	s_add_u32 s2, s2, 0xc000
	s_addc_u32 s3, s3, 0
	v_pk_fma_f32 v[124:125], v[94:95], v[10:11], v[124:125] op_sel:[1,0,0] op_sel_hi:[1,1,1]
	v_pk_fma_f32 v[126:127], v[94:95], v[12:13], v[126:127] op_sel:[1,0,0] op_sel_hi:[1,1,1]
	v_pk_fma_f32 v[128:129], v[94:95], v[14:15], v[128:129] op_sel:[1,0,0] op_sel_hi:[1,1,1]
	v_pk_fma_f32 v[122:123], v[94:95], v[16:17], v[122:123] op_sel:[1,0,0] op_sel_hi:[1,1,1]
	ds_read_b128 v[10:13], v43 offset:1696
	ds_read_b128 v[14:17], v43 offset:1712
	s_waitcnt vmcnt(62) lgkmcnt(6)
	global_load_dword v95, v110, s[2:3]
	s_add_u32 s2, s2, 0xc000
	s_addc_u32 s3, s3, 0
	v_pk_fma_f32 v[124:125], v[96:97], v[18:19], v[124:125] op_sel_hi:[0,1,1]
	v_pk_fma_f32 v[126:127], v[96:97], v[20:21], v[126:127] op_sel_hi:[0,1,1]
	v_pk_fma_f32 v[128:129], v[96:97], v[22:23], v[128:129] op_sel_hi:[0,1,1]
	v_pk_fma_f32 v[122:123], v[96:97], v[24:25], v[122:123] op_sel_hi:[0,1,1]
	ds_read_b128 v[18:21], v43 offset:1728
	ds_read_b128 v[22:25], v43 offset:1744
	s_waitcnt vmcnt(62) lgkmcnt(6)
	global_load_dword v96, v110, s[2:3]
	s_add_u32 s2, s2, 0xc000
	s_addc_u32 s3, s3, 0
	v_pk_fma_f32 v[124:125], v[96:97], v[26:27], v[124:125] op_sel:[1,0,0] op_sel_hi:[1,1,1]
	v_pk_fma_f32 v[126:127], v[96:97], v[28:29], v[126:127] op_sel:[1,0,0] op_sel_hi:[1,1,1]
	v_pk_fma_f32 v[128:129], v[96:97], v[30:31], v[128:129] op_sel:[1,0,0] op_sel_hi:[1,1,1]
	v_pk_fma_f32 v[122:123], v[96:97], v[32:33], v[122:123] op_sel:[1,0,0] op_sel_hi:[1,1,1]
	ds_read_b128 v[26:29], v43 offset:1760
	ds_read_b128 v[30:33], v43 offset:1776
	s_waitcnt vmcnt(62) lgkmcnt(6)
	global_load_dword v97, v110, s[2:3]
	s_add_u32 s2, s2, 0xc000
	s_addc_u32 s3, s3, 0
	v_pk_fma_f32 v[124:125], v[98:99], v[2:3], v[124:125] op_sel_hi:[0,1,1]
	v_pk_fma_f32 v[126:127], v[98:99], v[4:5], v[126:127] op_sel_hi:[0,1,1]
	v_pk_fma_f32 v[128:129], v[98:99], v[6:7], v[128:129] op_sel_hi:[0,1,1]
	v_pk_fma_f32 v[122:123], v[98:99], v[8:9], v[122:123] op_sel_hi:[0,1,1]
	ds_read_b128 v[2:5], v43 offset:1792
	ds_read_b128 v[6:9], v43 offset:1808
	s_waitcnt vmcnt(62) lgkmcnt(6)
	global_load_dword v98, v110, s[2:3]
	s_add_u32 s2, s2, 0xc000
	s_addc_u32 s3, s3, 0
	v_pk_fma_f32 v[124:125], v[98:99], v[10:11], v[124:125] op_sel:[1,0,0] op_sel_hi:[1,1,1]
	v_pk_fma_f32 v[126:127], v[98:99], v[12:13], v[126:127] op_sel:[1,0,0] op_sel_hi:[1,1,1]
	v_pk_fma_f32 v[128:129], v[98:99], v[14:15], v[128:129] op_sel:[1,0,0] op_sel_hi:[1,1,1]
	v_pk_fma_f32 v[122:123], v[98:99], v[16:17], v[122:123] op_sel:[1,0,0] op_sel_hi:[1,1,1]
	ds_read_b128 v[10:13], v43 offset:1824
	ds_read_b128 v[14:17], v43 offset:1840
	s_waitcnt vmcnt(62) lgkmcnt(6)
	global_load_dword v99, v110, s[2:3]
	s_add_u32 s2, s2, 0xc000
	s_addc_u32 s3, s3, 0
	v_pk_fma_f32 v[124:125], v[100:101], v[18:19], v[124:125] op_sel_hi:[0,1,1]
	v_pk_fma_f32 v[126:127], v[100:101], v[20:21], v[126:127] op_sel_hi:[0,1,1]
	v_pk_fma_f32 v[128:129], v[100:101], v[22:23], v[128:129] op_sel_hi:[0,1,1]
	v_pk_fma_f32 v[122:123], v[100:101], v[24:25], v[122:123] op_sel_hi:[0,1,1]
	ds_read_b128 v[18:21], v43 offset:1856
	ds_read_b128 v[22:25], v43 offset:1872
	s_waitcnt vmcnt(62) lgkmcnt(6)
; #define LAS __attribute__((address_space(3)))
; __device__ __forceinline__ void ph0_adaln(const Args& a, LAS unsigned char* lds, int tid, int G, int bid) {
;     ...
;         for (int k = 0; k < 256; k += 64) {
;             float w[64];
; #pragma unroll
;             for (int q = 0; q < 64; ++q) w[q] = wp[(size_t)(k + q) * MODW];
; #pragma unroll
;             for (int q = 0; q < 64; ++q) { const f32x4 c0 = *(const LAS f32x4*)(cond + (kq * 256 + k + q) * 8), c1 = *(const LAS f32x4*)(cond + (kq * 256 + k + q) * 8 + 4);
;                 acc[0] += w[q] * c0[0]; acc[1] += w[q] * c0[1]; acc[2] += w[q] * c0[2]; acc[3] += w[q] * c0[3];
;                 acc[4] += w[q] * c1[0]; acc[5] += w[q] * c1[1]; acc[6] += w[q] * c1[2]; acc[7] += w[q] * c1[3]; }
	global_load_dword v100, v110, s[2:3]
	s_add_u32 s2, s2, 0xc000
	s_addc_u32 s3, s3, 0
	v_pk_fma_f32 v[124:125], v[100:101], v[26:27], v[124:125] op_sel:[1,0,0] op_sel_hi:[1,1,1]
	v_pk_fma_f32 v[126:127], v[100:101], v[28:29], v[126:127] op_sel:[1,0,0] op_sel_hi:[1,1,1]
	v_pk_fma_f32 v[128:129], v[100:101], v[30:31], v[128:129] op_sel:[1,0,0] op_sel_hi:[1,1,1]
	v_pk_fma_f32 v[122:123], v[100:101], v[32:33], v[122:123] op_sel:[1,0,0] op_sel_hi:[1,1,1]
	ds_read_b128 v[26:29], v43 offset:1888
	ds_read_b128 v[30:33], v43 offset:1904
	s_waitcnt vmcnt(62) lgkmcnt(6)
	global_load_dword v101, v110, s[2:3]
	s_add_u32 s2, s2, 0xc000
	s_addc_u32 s3, s3, 0
	v_pk_fma_f32 v[124:125], v[102:103], v[2:3], v[124:125] op_sel_hi:[0,1,1]
	v_pk_fma_f32 v[126:127], v[102:103], v[4:5], v[126:127] op_sel_hi:[0,1,1]
	v_pk_fma_f32 v[128:129], v[102:103], v[6:7], v[128:129] op_sel_hi:[0,1,1]
	v_pk_fma_f32 v[122:123], v[102:103], v[8:9], v[122:123] op_sel_hi:[0,1,1]
	ds_read_b128 v[2:5], v43 offset:1920
	ds_read_b128 v[6:9], v43 offset:1936
	s_waitcnt vmcnt(62) lgkmcnt(6)
	global_load_dword v102, v110, s[2:3]
	s_add_u32 s2, s2, 0xc000
	s_addc_u32 s3, s3, 0
	v_pk_fma_f32 v[124:125], v[102:103], v[10:11], v[124:125] op_sel:[1,0,0] op_sel_hi:[1,1,1]
	v_pk_fma_f32 v[126:127], v[102:103], v[12:13], v[126:127] op_sel:[1,0,0] op_sel_hi:[1,1,1]
	v_pk_fma_f32 v[128:129], v[102:103], v[14:15], v[128:129] op_sel:[1,0,0] op_sel_hi:[1,1,1]
	v_pk_fma_f32 v[122:123], v[102:103], v[16:17], v[122:123] op_sel:[1,0,0] op_sel_hi:[1,1,1]
	ds_read_b128 v[10:13], v43 offset:1952
	ds_read_b128 v[14:17], v43 offset:1968
	s_waitcnt vmcnt(62) lgkmcnt(6)
	global_load_dword v103, v110, s[2:3]
	s_add_u32 s2, s2, 0xc000
	s_addc_u32 s3, s3, 0
	v_pk_fma_f32 v[124:125], v[104:105], v[18:19], v[124:125] op_sel_hi:[0,1,1]
	v_pk_fma_f32 v[126:127], v[104:105], v[20:21], v[126:127] op_sel_hi:[0,1,1]
	v_pk_fma_f32 v[128:129], v[104:105], v[22:23], v[128:129] op_sel_hi:[0,1,1]
	v_pk_fma_f32 v[122:123], v[104:105], v[24:25], v[122:123] op_sel_hi:[0,1,1]
	ds_read_b128 v[18:21], v43 offset:1984
	ds_read_b128 v[22:25], v43 offset:2000
	s_waitcnt vmcnt(62) lgkmcnt(6)
	global_load_dword v104, v110, s[2:3]
	s_add_u32 s2, s2, 0xc000
	s_addc_u32 s3, s3, 0
	v_pk_fma_f32 v[124:125], v[104:105], v[26:27], v[124:125] op_sel:[1,0,0] op_sel_hi:[1,1,1]
	v_pk_fma_f32 v[126:127], v[104:105], v[28:29], v[126:127] op_sel:[1,0,0] op_sel_hi:[1,1,1]
	v_pk_fma_f32 v[128:129], v[104:105], v[30:31], v[128:129] op_sel:[1,0,0] op_sel_hi:[1,1,1]
	v_pk_fma_f32 v[122:123], v[104:105], v[32:33], v[122:123] op_sel:[1,0,0] op_sel_hi:[1,1,1]
	ds_read_b128 v[26:29], v43 offset:2016
	ds_read_b128 v[30:33], v43 offset:2032
	s_waitcnt vmcnt(62) lgkmcnt(6)
	global_load_dword v105, v110, s[2:3]
	s_add_u32 s2, s2, 0xc000
	s_addc_u32 s3, s3, 0
	v_pk_fma_f32 v[124:125], v[106:107], v[2:3], v[124:125] op_sel_hi:[0,1,1]
	v_pk_fma_f32 v[126:127], v[106:107], v[4:5], v[126:127] op_sel_hi:[0,1,1]
	v_pk_fma_f32 v[128:129], v[106:107], v[6:7], v[128:129] op_sel_hi:[0,1,1]
	v_pk_fma_f32 v[122:123], v[106:107], v[8:9], v[122:123] op_sel_hi:[0,1,1]
	ds_read_b128 v[2:5], v43 offset:2048
	ds_read_b128 v[6:9], v43 offset:2064
	s_waitcnt vmcnt(62) lgkmcnt(6)
	global_load_dword v106, v110, s[2:3]
	s_add_u32 s2, s2, 0xc000
	s_addc_u32 s3, s3, 0
	v_pk_fma_f32 v[124:125], v[106:107], v[10:11], v[124:125] op_sel:[1,0,0] op_sel_hi:[1,1,1]
	v_pk_fma_f32 v[126:127], v[106:107], v[12:13], v[126:127] op_sel:[1,0,0] op_sel_hi:[1,1,1]
	v_pk_fma_f32 v[128:129], v[106:107], v[14:15], v[128:129] op_sel:[1,0,0] op_sel_hi:[1,1,1]
	v_pk_fma_f32 v[122:123], v[106:107], v[16:17], v[122:123] op_sel:[1,0,0] op_sel_hi:[1,1,1]
	ds_read_b128 v[10:13], v43 offset:2080
	ds_read_b128 v[14:17], v43 offset:2096
	s_waitcnt vmcnt(62) lgkmcnt(6)
	global_load_dword v107, v110, s[2:3]
	s_add_u32 s2, s2, 0xc000
	s_addc_u32 s3, s3, 0
	v_pk_fma_f32 v[124:125], v[108:109], v[18:19], v[124:125] op_sel_hi:[0,1,1]
	v_pk_fma_f32 v[126:127], v[108:109], v[20:21], v[126:127] op_sel_hi:[0,1,1]
	v_pk_fma_f32 v[128:129], v[108:109], v[22:23], v[128:129] op_sel_hi:[0,1,1]
	v_pk_fma_f32 v[122:123], v[108:109], v[24:25], v[122:123] op_sel_hi:[0,1,1]
	ds_read_b128 v[18:21], v43 offset:2112
	ds_read_b128 v[22:25], v43 offset:2128
	s_waitcnt vmcnt(62) lgkmcnt(6)
	global_load_dword v108, v110, s[2:3]
	s_add_u32 s2, s2, 0xc000
	s_addc_u32 s3, s3, 0
	v_pk_fma_f32 v[124:125], v[108:109], v[26:27], v[124:125] op_sel:[1,0,0] op_sel_hi:[1,1,1]
	v_pk_fma_f32 v[126:127], v[108:109], v[28:29], v[126:127] op_sel:[1,0,0] op_sel_hi:[1,1,1]
	v_pk_fma_f32 v[128:129], v[108:109], v[30:31], v[128:129] op_sel:[1,0,0] op_sel_hi:[1,1,1]
	v_pk_fma_f32 v[122:123], v[108:109], v[32:33], v[122:123] op_sel:[1,0,0] op_sel_hi:[1,1,1]
	ds_read_b128 v[26:29], v43 offset:2144
	ds_read_b128 v[30:33], v43 offset:2160
	v_add_u32_e32 v43, 0x800, v43
	s_add_i32 s4, s4, -1
	s_cmp_lg_u32 s4, 0
	s_cbranch_scc1 .Lada_kloop
; #define LAS __attribute__((address_space(3)))
; __device__ __forceinline__ void ph0_adaln(const Args& a, LAS unsigned char* lds, int tid, int G, int bid) {
;     ...
;         for (int k = 0; k < 256; k += 64) {
;             float w[64];
; #pragma unroll
;             for (int q = 0; q < 64; ++q) w[q] = wp[(size_t)(k + q) * MODW];
; #pragma unroll
;             for (int q = 0; q < 64; ++q) { const f32x4 c0 = *(const LAS f32x4*)(cond + (kq * 256 + k + q) * 8), c1 = *(const LAS f32x4*)(cond + (kq * 256 + k + q) * 8 + 4);
;                 acc[0] += w[q] * c0[0]; acc[1] += w[q] * c0[1]; acc[2] += w[q] * c0[2]; acc[3] += w[q] * c0[3];
;                 acc[4] += w[q] * c1[0]; acc[5] += w[q] * c1[1]; acc[6] += w[q] * c1[2]; acc[7] += w[q] * c1[3]; }
	s_waitcnt vmcnt(62) lgkmcnt(6)
	global_load_dword v109, v110, s[2:3]
	s_add_u32 s2, s2, 0xc000
	s_addc_u32 s3, s3, 0
	v_pk_fma_f32 v[124:125], v[46:47], v[2:3], v[124:125] op_sel_hi:[0,1,1]
	v_pk_fma_f32 v[126:127], v[46:47], v[4:5], v[126:127] op_sel_hi:[0,1,1]
	v_pk_fma_f32 v[128:129], v[46:47], v[6:7], v[128:129] op_sel_hi:[0,1,1]
	v_pk_fma_f32 v[122:123], v[46:47], v[8:9], v[122:123] op_sel_hi:[0,1,1]
	ds_read_b128 v[2:5], v43 offset:128
	ds_read_b128 v[6:9], v43 offset:144
	s_waitcnt vmcnt(62) lgkmcnt(6)
	v_pk_fma_f32 v[124:125], v[46:47], v[10:11], v[124:125] op_sel:[1,0,0] op_sel_hi:[1,1,1]
	v_pk_fma_f32 v[126:127], v[46:47], v[12:13], v[126:127] op_sel:[1,0,0] op_sel_hi:[1,1,1]
	v_pk_fma_f32 v[128:129], v[46:47], v[14:15], v[128:129] op_sel:[1,0,0] op_sel_hi:[1,1,1]
	v_pk_fma_f32 v[122:123], v[46:47], v[16:17], v[122:123] op_sel:[1,0,0] op_sel_hi:[1,1,1]
	ds_read_b128 v[10:13], v43 offset:160
	ds_read_b128 v[14:17], v43 offset:176
	s_waitcnt vmcnt(61) lgkmcnt(6)
	v_pk_fma_f32 v[124:125], v[48:49], v[18:19], v[124:125] op_sel_hi:[0,1,1]
	v_pk_fma_f32 v[126:127], v[48:49], v[20:21], v[126:127] op_sel_hi:[0,1,1]
	v_pk_fma_f32 v[128:129], v[48:49], v[22:23], v[128:129] op_sel_hi:[0,1,1]
	v_pk_fma_f32 v[122:123], v[48:49], v[24:25], v[122:123] op_sel_hi:[0,1,1]
	ds_read_b128 v[18:21], v43 offset:192
	ds_read_b128 v[22:25], v43 offset:208
	s_waitcnt vmcnt(60) lgkmcnt(6)
	v_pk_fma_f32 v[124:125], v[48:49], v[26:27], v[124:125] op_sel:[1,0,0] op_sel_hi:[1,1,1]
	v_pk_fma_f32 v[126:127], v[48:49], v[28:29], v[126:127] op_sel:[1,0,0] op_sel_hi:[1,1,1]
	v_pk_fma_f32 v[128:129], v[48:49], v[30:31], v[128:129] op_sel:[1,0,0] op_sel_hi:[1,1,1]
	v_pk_fma_f32 v[122:123], v[48:49], v[32:33], v[122:123] op_sel:[1,0,0] op_sel_hi:[1,1,1]
	ds_read_b128 v[26:29], v43 offset:224
	ds_read_b128 v[30:33], v43 offset:240
	s_waitcnt vmcnt(59) lgkmcnt(6)
	v_pk_fma_f32 v[124:125], v[50:51], v[2:3], v[124:125] op_sel_hi:[0,1,1]
	v_pk_fma_f32 v[126:127], v[50:51], v[4:5], v[126:127] op_sel_hi:[0,1,1]
	v_pk_fma_f32 v[128:129], v[50:51], v[6:7], v[128:129] op_sel_hi:[0,1,1]
	v_pk_fma_f32 v[122:123], v[50:51], v[8:9], v[122:123] op_sel_hi:[0,1,1]
	ds_read_b128 v[2:5], v43 offset:256
	ds_read_b128 v[6:9], v43 offset:272
	s_waitcnt vmcnt(58) lgkmcnt(6)
	v_pk_fma_f32 v[124:125], v[50:51], v[10:11], v[124:125] op_sel:[1,0,0] op_sel_hi:[1,1,1]
	v_pk_fma_f32 v[126:127], v[50:51], v[12:13], v[126:127] op_sel:[1,0,0] op_sel_hi:[1,1,1]
	v_pk_fma_f32 v[128:129], v[50:51], v[14:15], v[128:129] op_sel:[1,0,0] op_sel_hi:[1,1,1]
	v_pk_fma_f32 v[122:123], v[50:51], v[16:17], v[122:123] op_sel:[1,0,0] op_sel_hi:[1,1,1]
	ds_read_b128 v[10:13], v43 offset:288
	ds_read_b128 v[14:17], v43 offset:304
	s_waitcnt vmcnt(57) lgkmcnt(6)
	v_pk_fma_f32 v[124:125], v[52:53], v[18:19], v[124:125] op_sel_hi:[0,1,1]
	v_pk_fma_f32 v[126:127], v[52:53], v[20:21], v[126:127] op_sel_hi:[0,1,1]
	v_pk_fma_f32 v[128:129], v[52:53], v[22:23], v[128:129] op_sel_hi:[0,1,1]
	v_pk_fma_f32 v[122:123], v[52:53], v[24:25], v[122:123] op_sel_hi:[0,1,1]
	ds_read_b128 v[18:21], v43 offset:320
	ds_read_b128 v[22:25], v43 offset:336
	s_waitcnt vmcnt(56) lgkmcnt(6)
	v_pk_fma_f32 v[124:125], v[52:53], v[26:27], v[124:125] op_sel:[1,0,0] op_sel_hi:[1,1,1]
	v_pk_fma_f32 v[126:127], v[52:53], v[28:29], v[126:127] op_sel:[1,0,0] op_sel_hi:[1,1,1]
	v_pk_fma_f32 v[128:129], v[52:53], v[30:31], v[128:129] op_sel:[1,0,0] op_sel_hi:[1,1,1]
	v_pk_fma_f32 v[122:123], v[52:53], v[32:33], v[122:123] op_sel:[1,0,0] op_sel_hi:[1,1,1]
	ds_read_b128 v[26:29], v43 offset:352
	ds_read_b128 v[30:33], v43 offset:368
	s_waitcnt vmcnt(55) lgkmcnt(6)
	v_pk_fma_f32 v[124:125], v[54:55], v[2:3], v[124:125] op_sel_hi:[0,1,1]
	v_pk_fma_f32 v[126:127], v[54:55], v[4:5], v[126:127] op_sel_hi:[0,1,1]
	v_pk_fma_f32 v[128:129], v[54:55], v[6:7], v[128:129] op_sel_hi:[0,1,1]
	v_pk_fma_f32 v[122:123], v[54:55], v[8:9], v[122:123] op_sel_hi:[0,1,1]
	ds_read_b128 v[2:5], v43 offset:384
	ds_read_b128 v[6:9], v43 offset:400
	s_waitcnt vmcnt(54) lgkmcnt(6)
	v_pk_fma_f32 v[124:125], v[54:55], v[10:11], v[124:125] op_sel:[1,0,0] op_sel_hi:[1,1,1]
	v_pk_fma_f32 v[126:127], v[54:55], v[12:13], v[126:127] op_sel:[1,0,0] op_sel_hi:[1,1,1]
	v_pk_fma_f32 v[128:129], v[54:55], v[14:15], v[128:129] op_sel:[1,0,0] op_sel_hi:[1,1,1]
	v_pk_fma_f32 v[122:123], v[54:55], v[16:17], v[122:123] op_sel:[1,0,0] op_sel_hi:[1,1,1]
	ds_read_b128 v[10:13], v43 offset:416
	ds_read_b128 v[14:17], v43 offset:432
	s_waitcnt vmcnt(53) lgkmcnt(6)
	v_pk_fma_f32 v[124:125], v[56:57], v[18:19], v[124:125] op_sel_hi:[0,1,1]
	v_pk_fma_f32 v[126:127], v[56:57], v[20:21], v[126:127] op_sel_hi:[0,1,1]
	v_pk_fma_f32 v[128:129], v[56:57], v[22:23], v[128:129] op_sel_hi:[0,1,1]
	v_pk_fma_f32 v[122:123], v[56:57], v[24:25], v[122:123] op_sel_hi:[0,1,1]
	ds_read_b128 v[18:21], v43 offset:448
	ds_read_b128 v[22:25], v43 offset:464
	s_waitcnt vmcnt(52) lgkmcnt(6)
	v_pk_fma_f32 v[124:125], v[56:57], v[26:27], v[124:125] op_sel:[1,0,0] op_sel_hi:[1,1,1]
	v_pk_fma_f32 v[126:127], v[56:57], v[28:29], v[126:127] op_sel:[1,0,0] op_sel_hi:[1,1,1]
	v_pk_fma_f32 v[128:129], v[56:57], v[30:31], v[128:129] op_sel:[1,0,0] op_sel_hi:[1,1,1]
	v_pk_fma_f32 v[122:123], v[56:57], v[32:33], v[122:123] op_sel:[1,0,0] op_sel_hi:[1,1,1]
	ds_read_b128 v[26:29], v43 offset:480
	ds_read_b128 v[30:33], v43 offset:496
	s_waitcnt vmcnt(51) lgkmcnt(6)
	v_pk_fma_f32 v[124:125], v[58:59], v[2:3], v[124:125] op_sel_hi:[0,1,1]
	v_pk_fma_f32 v[126:127], v[58:59], v[4:5], v[126:127] op_sel_hi:[0,1,1]
	v_pk_fma_f32 v[128:129], v[58:59], v[6:7], v[128:129] op_sel_hi:[0,1,1]
	v_pk_fma_f32 v[122:123], v[58:59], v[8:9], v[122:123] op_sel_hi:[0,1,1]
	ds_read_b128 v[2:5], v43 offset:512
	ds_read_b128 v[6:9], v43 offset:528
	s_waitcnt vmcnt(50) lgkmcnt(6)
; #define LAS __attribute__((address_space(3)))
; __device__ __forceinline__ void ph0_adaln(const Args& a, LAS unsigned char* lds, int tid, int G, int bid) {
;     ...
;         for (int k = 0; k < 256; k += 64) {
;             float w[64];
; #pragma unroll
;             for (int q = 0; q < 64; ++q) w[q] = wp[(size_t)(k + q) * MODW];
; #pragma unroll
;             for (int q = 0; q < 64; ++q) { const f32x4 c0 = *(const LAS f32x4*)(cond + (kq * 256 + k + q) * 8), c1 = *(const LAS f32x4*)(cond + (kq * 256 + k + q) * 8 + 4);
;                 acc[0] += w[q] * c0[0]; acc[1] += w[q] * c0[1]; acc[2] += w[q] * c0[2]; acc[3] += w[q] * c0[3];
;                 acc[4] += w[q] * c1[0]; acc[5] += w[q] * c1[1]; acc[6] += w[q] * c1[2]; acc[7] += w[q] * c1[3]; }
	v_pk_fma_f32 v[124:125], v[58:59], v[10:11], v[124:125] op_sel:[1,0,0] op_sel_hi:[1,1,1]
	v_pk_fma_f32 v[126:127], v[58:59], v[12:13], v[126:127] op_sel:[1,0,0] op_sel_hi:[1,1,1]
	v_pk_fma_f32 v[128:129], v[58:59], v[14:15], v[128:129] op_sel:[1,0,0] op_sel_hi:[1,1,1]
	v_pk_fma_f32 v[122:123], v[58:59], v[16:17], v[122:123] op_sel:[1,0,0] op_sel_hi:[1,1,1]
	ds_read_b128 v[10:13], v43 offset:544
	ds_read_b128 v[14:17], v43 offset:560
	s_waitcnt vmcnt(49) lgkmcnt(6)
	v_pk_fma_f32 v[124:125], v[60:61], v[18:19], v[124:125] op_sel_hi:[0,1,1]
	v_pk_fma_f32 v[126:127], v[60:61], v[20:21], v[126:127] op_sel_hi:[0,1,1]
	v_pk_fma_f32 v[128:129], v[60:61], v[22:23], v[128:129] op_sel_hi:[0,1,1]
	v_pk_fma_f32 v[122:123], v[60:61], v[24:25], v[122:123] op_sel_hi:[0,1,1]
	ds_read_b128 v[18:21], v43 offset:576
	ds_read_b128 v[22:25], v43 offset:592
	s_waitcnt vmcnt(48) lgkmcnt(6)
	v_pk_fma_f32 v[124:125], v[60:61], v[26:27], v[124:125] op_sel:[1,0,0] op_sel_hi:[1,1,1]
	v_pk_fma_f32 v[126:127], v[60:61], v[28:29], v[126:127] op_sel:[1,0,0] op_sel_hi:[1,1,1]
	v_pk_fma_f32 v[128:129], v[60:61], v[30:31], v[128:129] op_sel:[1,0,0] op_sel_hi:[1,1,1]
	v_pk_fma_f32 v[122:123], v[60:61], v[32:33], v[122:123] op_sel:[1,0,0] op_sel_hi:[1,1,1]
	ds_read_b128 v[26:29], v43 offset:608
	ds_read_b128 v[30:33], v43 offset:624
	s_waitcnt vmcnt(47) lgkmcnt(6)
	v_pk_fma_f32 v[124:125], v[62:63], v[2:3], v[124:125] op_sel_hi:[0,1,1]
	v_pk_fma_f32 v[126:127], v[62:63], v[4:5], v[126:127] op_sel_hi:[0,1,1]
	v_pk_fma_f32 v[128:129], v[62:63], v[6:7], v[128:129] op_sel_hi:[0,1,1]
	v_pk_fma_f32 v[122:123], v[62:63], v[8:9], v[122:123] op_sel_hi:[0,1,1]
	ds_read_b128 v[2:5], v43 offset:640
	ds_read_b128 v[6:9], v43 offset:656
	s_waitcnt vmcnt(46) lgkmcnt(6)
	v_pk_fma_f32 v[124:125], v[62:63], v[10:11], v[124:125] op_sel:[1,0,0] op_sel_hi:[1,1,1]
	v_pk_fma_f32 v[126:127], v[62:63], v[12:13], v[126:127] op_sel:[1,0,0] op_sel_hi:[1,1,1]
	v_pk_fma_f32 v[128:129], v[62:63], v[14:15], v[128:129] op_sel:[1,0,0] op_sel_hi:[1,1,1]
	v_pk_fma_f32 v[122:123], v[62:63], v[16:17], v[122:123] op_sel:[1,0,0] op_sel_hi:[1,1,1]
	ds_read_b128 v[10:13], v43 offset:672
	ds_read_b128 v[14:17], v43 offset:688
	s_waitcnt vmcnt(45) lgkmcnt(6)
	v_pk_fma_f32 v[124:125], v[64:65], v[18:19], v[124:125] op_sel_hi:[0,1,1]
	v_pk_fma_f32 v[126:127], v[64:65], v[20:21], v[126:127] op_sel_hi:[0,1,1]
	v_pk_fma_f32 v[128:129], v[64:65], v[22:23], v[128:129] op_sel_hi:[0,1,1]
	v_pk_fma_f32 v[122:123], v[64:65], v[24:25], v[122:123] op_sel_hi:[0,1,1]
	ds_read_b128 v[18:21], v43 offset:704
	ds_read_b128 v[22:25], v43 offset:720
	s_waitcnt vmcnt(44) lgkmcnt(6)
	v_pk_fma_f32 v[124:125], v[64:65], v[26:27], v[124:125] op_sel:[1,0,0] op_sel_hi:[1,1,1]
	v_pk_fma_f32 v[126:127], v[64:65], v[28:29], v[126:127] op_sel:[1,0,0] op_sel_hi:[1,1,1]
	v_pk_fma_f32 v[128:129], v[64:65], v[30:31], v[128:129] op_sel:[1,0,0] op_sel_hi:[1,1,1]
	v_pk_fma_f32 v[122:123], v[64:65], v[32:33], v[122:123] op_sel:[1,0,0] op_sel_hi:[1,1,1]
	ds_read_b128 v[26:29], v43 offset:736
	ds_read_b128 v[30:33], v43 offset:752
	s_waitcnt vmcnt(43) lgkmcnt(6)
	v_pk_fma_f32 v[124:125], v[66:67], v[2:3], v[124:125] op_sel_hi:[0,1,1]
	v_pk_fma_f32 v[126:127], v[66:67], v[4:5], v[126:127] op_sel_hi:[0,1,1]
	v_pk_fma_f32 v[128:129], v[66:67], v[6:7], v[128:129] op_sel_hi:[0,1,1]
	v_pk_fma_f32 v[122:123], v[66:67], v[8:9], v[122:123] op_sel_hi:[0,1,1]
	ds_read_b128 v[2:5], v43 offset:768
	ds_read_b128 v[6:9], v43 offset:784
	s_waitcnt vmcnt(42) lgkmcnt(6)
	v_pk_fma_f32 v[124:125], v[66:67], v[10:11], v[124:125] op_sel:[1,0,0] op_sel_hi:[1,1,1]
	v_pk_fma_f32 v[126:127], v[66:67], v[12:13], v[126:127] op_sel:[1,0,0] op_sel_hi:[1,1,1]
	v_pk_fma_f32 v[128:129], v[66:67], v[14:15], v[128:129] op_sel:[1,0,0] op_sel_hi:[1,1,1]
	v_pk_fma_f32 v[122:123], v[66:67], v[16:17], v[122:123] op_sel:[1,0,0] op_sel_hi:[1,1,1]
	ds_read_b128 v[10:13], v43 offset:800
	ds_read_b128 v[14:17], v43 offset:816
	s_waitcnt vmcnt(41) lgkmcnt(6)
	v_pk_fma_f32 v[124:125], v[68:69], v[18:19], v[124:125] op_sel_hi:[0,1,1]
	v_pk_fma_f32 v[126:127], v[68:69], v[20:21], v[126:127] op_sel_hi:[0,1,1]
	v_pk_fma_f32 v[128:129], v[68:69], v[22:23], v[128:129] op_sel_hi:[0,1,1]
	v_pk_fma_f32 v[122:123], v[68:69], v[24:25], v[122:123] op_sel_hi:[0,1,1]
	ds_read_b128 v[18:21], v43 offset:832
	ds_read_b128 v[22:25], v43 offset:848
	s_waitcnt vmcnt(40) lgkmcnt(6)
	v_pk_fma_f32 v[124:125], v[68:69], v[26:27], v[124:125] op_sel:[1,0,0] op_sel_hi:[1,1,1]
	v_pk_fma_f32 v[126:127], v[68:69], v[28:29], v[126:127] op_sel:[1,0,0] op_sel_hi:[1,1,1]
	v_pk_fma_f32 v[128:129], v[68:69], v[30:31], v[128:129] op_sel:[1,0,0] op_sel_hi:[1,1,1]
	v_pk_fma_f32 v[122:123], v[68:69], v[32:33], v[122:123] op_sel:[1,0,0] op_sel_hi:[1,1,1]
	ds_read_b128 v[26:29], v43 offset:864
	ds_read_b128 v[30:33], v43 offset:880
	s_waitcnt vmcnt(39) lgkmcnt(6)
	v_pk_fma_f32 v[124:125], v[70:71], v[2:3], v[124:125] op_sel_hi:[0,1,1]
	v_pk_fma_f32 v[126:127], v[70:71], v[4:5], v[126:127] op_sel_hi:[0,1,1]
	v_pk_fma_f32 v[128:129], v[70:71], v[6:7], v[128:129] op_sel_hi:[0,1,1]
	v_pk_fma_f32 v[122:123], v[70:71], v[8:9], v[122:123] op_sel_hi:[0,1,1]
	ds_read_b128 v[2:5], v43 offset:896
	ds_read_b128 v[6:9], v43 offset:912
	s_waitcnt vmcnt(38) lgkmcnt(6)
	v_pk_fma_f32 v[124:125], v[70:71], v[10:11], v[124:125] op_sel:[1,0,0] op_sel_hi:[1,1,1]
	v_pk_fma_f32 v[126:127], v[70:71], v[12:13], v[126:127] op_sel:[1,0,0] op_sel_hi:[1,1,1]
	v_pk_fma_f32 v[128:129], v[70:71], v[14:15], v[128:129] op_sel:[1,0,0] op_sel_hi:[1,1,1]
	v_pk_fma_f32 v[122:123], v[70:71], v[16:17], v[122:123] op_sel:[1,0,0] op_sel_hi:[1,1,1]
	ds_read_b128 v[10:13], v43 offset:928
	ds_read_b128 v[14:17], v43 offset:944
	s_waitcnt vmcnt(37) lgkmcnt(6)
; #define LAS __attribute__((address_space(3)))
; __device__ __forceinline__ void ph0_adaln(const Args& a, LAS unsigned char* lds, int tid, int G, int bid) {
;     ...
;         for (int k = 0; k < 256; k += 64) {
;             float w[64];
; #pragma unroll
;             for (int q = 0; q < 64; ++q) w[q] = wp[(size_t)(k + q) * MODW];
; #pragma unroll
;             for (int q = 0; q < 64; ++q) { const f32x4 c0 = *(const LAS f32x4*)(cond + (kq * 256 + k + q) * 8), c1 = *(const LAS f32x4*)(cond + (kq * 256 + k + q) * 8 + 4);
;                 acc[0] += w[q] * c0[0]; acc[1] += w[q] * c0[1]; acc[2] += w[q] * c0[2]; acc[3] += w[q] * c0[3];
;                 acc[4] += w[q] * c1[0]; acc[5] += w[q] * c1[1]; acc[6] += w[q] * c1[2]; acc[7] += w[q] * c1[3]; }
	v_pk_fma_f32 v[124:125], v[72:73], v[18:19], v[124:125] op_sel_hi:[0,1,1]
	v_pk_fma_f32 v[126:127], v[72:73], v[20:21], v[126:127] op_sel_hi:[0,1,1]
	v_pk_fma_f32 v[128:129], v[72:73], v[22:23], v[128:129] op_sel_hi:[0,1,1]
	v_pk_fma_f32 v[122:123], v[72:73], v[24:25], v[122:123] op_sel_hi:[0,1,1]
	ds_read_b128 v[18:21], v43 offset:960
	ds_read_b128 v[22:25], v43 offset:976
	s_waitcnt vmcnt(36) lgkmcnt(6)
	v_pk_fma_f32 v[124:125], v[72:73], v[26:27], v[124:125] op_sel:[1,0,0] op_sel_hi:[1,1,1]
	v_pk_fma_f32 v[126:127], v[72:73], v[28:29], v[126:127] op_sel:[1,0,0] op_sel_hi:[1,1,1]
	v_pk_fma_f32 v[128:129], v[72:73], v[30:31], v[128:129] op_sel:[1,0,0] op_sel_hi:[1,1,1]
	v_pk_fma_f32 v[122:123], v[72:73], v[32:33], v[122:123] op_sel:[1,0,0] op_sel_hi:[1,1,1]
	ds_read_b128 v[26:29], v43 offset:992
	ds_read_b128 v[30:33], v43 offset:1008
	s_waitcnt vmcnt(35) lgkmcnt(6)
	v_pk_fma_f32 v[124:125], v[74:75], v[2:3], v[124:125] op_sel_hi:[0,1,1]
	v_pk_fma_f32 v[126:127], v[74:75], v[4:5], v[126:127] op_sel_hi:[0,1,1]
	v_pk_fma_f32 v[128:129], v[74:75], v[6:7], v[128:129] op_sel_hi:[0,1,1]
	v_pk_fma_f32 v[122:123], v[74:75], v[8:9], v[122:123] op_sel_hi:[0,1,1]
	ds_read_b128 v[2:5], v43 offset:1024
	ds_read_b128 v[6:9], v43 offset:1040
	s_waitcnt vmcnt(34) lgkmcnt(6)
	v_pk_fma_f32 v[124:125], v[74:75], v[10:11], v[124:125] op_sel:[1,0,0] op_sel_hi:[1,1,1]
	v_pk_fma_f32 v[126:127], v[74:75], v[12:13], v[126:127] op_sel:[1,0,0] op_sel_hi:[1,1,1]
	v_pk_fma_f32 v[128:129], v[74:75], v[14:15], v[128:129] op_sel:[1,0,0] op_sel_hi:[1,1,1]
	v_pk_fma_f32 v[122:123], v[74:75], v[16:17], v[122:123] op_sel:[1,0,0] op_sel_hi:[1,1,1]
	ds_read_b128 v[10:13], v43 offset:1056
	ds_read_b128 v[14:17], v43 offset:1072
	s_waitcnt vmcnt(33) lgkmcnt(6)
	v_pk_fma_f32 v[124:125], v[76:77], v[18:19], v[124:125] op_sel_hi:[0,1,1]
	v_pk_fma_f32 v[126:127], v[76:77], v[20:21], v[126:127] op_sel_hi:[0,1,1]
	v_pk_fma_f32 v[128:129], v[76:77], v[22:23], v[128:129] op_sel_hi:[0,1,1]
	v_pk_fma_f32 v[122:123], v[76:77], v[24:25], v[122:123] op_sel_hi:[0,1,1]
	ds_read_b128 v[18:21], v43 offset:1088
	ds_read_b128 v[22:25], v43 offset:1104
	s_waitcnt vmcnt(32) lgkmcnt(6)
	v_pk_fma_f32 v[124:125], v[76:77], v[26:27], v[124:125] op_sel:[1,0,0] op_sel_hi:[1,1,1]
	v_pk_fma_f32 v[126:127], v[76:77], v[28:29], v[126:127] op_sel:[1,0,0] op_sel_hi:[1,1,1]
	v_pk_fma_f32 v[128:129], v[76:77], v[30:31], v[128:129] op_sel:[1,0,0] op_sel_hi:[1,1,1]
	v_pk_fma_f32 v[122:123], v[76:77], v[32:33], v[122:123] op_sel:[1,0,0] op_sel_hi:[1,1,1]
	ds_read_b128 v[26:29], v43 offset:1120
	ds_read_b128 v[30:33], v43 offset:1136
	s_waitcnt vmcnt(31) lgkmcnt(6)
	v_pk_fma_f32 v[124:125], v[78:79], v[2:3], v[124:125] op_sel_hi:[0,1,1]
	v_pk_fma_f32 v[126:127], v[78:79], v[4:5], v[126:127] op_sel_hi:[0,1,1]
	v_pk_fma_f32 v[128:129], v[78:79], v[6:7], v[128:129] op_sel_hi:[0,1,1]
	v_pk_fma_f32 v[122:123], v[78:79], v[8:9], v[122:123] op_sel_hi:[0,1,1]
	ds_read_b128 v[2:5], v43 offset:1152
	ds_read_b128 v[6:9], v43 offset:1168
	s_waitcnt vmcnt(30) lgkmcnt(6)
	v_pk_fma_f32 v[124:125], v[78:79], v[10:11], v[124:125] op_sel:[1,0,0] op_sel_hi:[1,1,1]
	v_pk_fma_f32 v[126:127], v[78:79], v[12:13], v[126:127] op_sel:[1,0,0] op_sel_hi:[1,1,1]
	v_pk_fma_f32 v[128:129], v[78:79], v[14:15], v[128:129] op_sel:[1,0,0] op_sel_hi:[1,1,1]
	v_pk_fma_f32 v[122:123], v[78:79], v[16:17], v[122:123] op_sel:[1,0,0] op_sel_hi:[1,1,1]
	ds_read_b128 v[10:13], v43 offset:1184
	ds_read_b128 v[14:17], v43 offset:1200
	s_waitcnt vmcnt(29) lgkmcnt(6)
	v_pk_fma_f32 v[124:125], v[80:81], v[18:19], v[124:125] op_sel_hi:[0,1,1]
	v_pk_fma_f32 v[126:127], v[80:81], v[20:21], v[126:127] op_sel_hi:[0,1,1]
	v_pk_fma_f32 v[128:129], v[80:81], v[22:23], v[128:129] op_sel_hi:[0,1,1]
	v_pk_fma_f32 v[122:123], v[80:81], v[24:25], v[122:123] op_sel_hi:[0,1,1]
	ds_read_b128 v[18:21], v43 offset:1216
	ds_read_b128 v[22:25], v43 offset:1232
	s_waitcnt vmcnt(28) lgkmcnt(6)
	v_pk_fma_f32 v[124:125], v[80:81], v[26:27], v[124:125] op_sel:[1,0,0] op_sel_hi:[1,1,1]
	v_pk_fma_f32 v[126:127], v[80:81], v[28:29], v[126:127] op_sel:[1,0,0] op_sel_hi:[1,1,1]
	v_pk_fma_f32 v[128:129], v[80:81], v[30:31], v[128:129] op_sel:[1,0,0] op_sel_hi:[1,1,1]
	v_pk_fma_f32 v[122:123], v[80:81], v[32:33], v[122:123] op_sel:[1,0,0] op_sel_hi:[1,1,1]
	ds_read_b128 v[26:29], v43 offset:1248
	ds_read_b128 v[30:33], v43 offset:1264
	s_waitcnt vmcnt(27) lgkmcnt(6)
	v_pk_fma_f32 v[124:125], v[82:83], v[2:3], v[124:125] op_sel_hi:[0,1,1]
	v_pk_fma_f32 v[126:127], v[82:83], v[4:5], v[126:127] op_sel_hi:[0,1,1]
	v_pk_fma_f32 v[128:129], v[82:83], v[6:7], v[128:129] op_sel_hi:[0,1,1]
	v_pk_fma_f32 v[122:123], v[82:83], v[8:9], v[122:123] op_sel_hi:[0,1,1]
	ds_read_b128 v[2:5], v43 offset:1280
	ds_read_b128 v[6:9], v43 offset:1296
	s_waitcnt vmcnt(26) lgkmcnt(6)
	v_pk_fma_f32 v[124:125], v[82:83], v[10:11], v[124:125] op_sel:[1,0,0] op_sel_hi:[1,1,1]
	v_pk_fma_f32 v[126:127], v[82:83], v[12:13], v[126:127] op_sel:[1,0,0] op_sel_hi:[1,1,1]
	v_pk_fma_f32 v[128:129], v[82:83], v[14:15], v[128:129] op_sel:[1,0,0] op_sel_hi:[1,1,1]
	v_pk_fma_f32 v[122:123], v[82:83], v[16:17], v[122:123] op_sel:[1,0,0] op_sel_hi:[1,1,1]
	ds_read_b128 v[10:13], v43 offset:1312
	ds_read_b128 v[14:17], v43 offset:1328
	s_waitcnt vmcnt(25) lgkmcnt(6)
	v_pk_fma_f32 v[124:125], v[84:85], v[18:19], v[124:125] op_sel_hi:[0,1,1]
	v_pk_fma_f32 v[126:127], v[84:85], v[20:21], v[126:127] op_sel_hi:[0,1,1]
	v_pk_fma_f32 v[128:129], v[84:85], v[22:23], v[128:129] op_sel_hi:[0,1,1]
	v_pk_fma_f32 v[122:123], v[84:85], v[24:25], v[122:123] op_sel_hi:[0,1,1]
	ds_read_b128 v[18:21], v43 offset:1344
	ds_read_b128 v[22:25], v43 offset:1360
	s_waitcnt vmcnt(24) lgkmcnt(6)
; #define LAS __attribute__((address_space(3)))
; __device__ __forceinline__ void ph0_adaln(const Args& a, LAS unsigned char* lds, int tid, int G, int bid) {
;     ...
;         for (int k = 0; k < 256; k += 64) {
;             float w[64];
; #pragma unroll
;             for (int q = 0; q < 64; ++q) w[q] = wp[(size_t)(k + q) * MODW];
; #pragma unroll
;             for (int q = 0; q < 64; ++q) { const f32x4 c0 = *(const LAS f32x4*)(cond + (kq * 256 + k + q) * 8), c1 = *(const LAS f32x4*)(cond + (kq * 256 + k + q) * 8 + 4);
;                 acc[0] += w[q] * c0[0]; acc[1] += w[q] * c0[1]; acc[2] += w[q] * c0[2]; acc[3] += w[q] * c0[3];
;                 acc[4] += w[q] * c1[0]; acc[5] += w[q] * c1[1]; acc[6] += w[q] * c1[2]; acc[7] += w[q] * c1[3]; }
	v_pk_fma_f32 v[124:125], v[84:85], v[26:27], v[124:125] op_sel:[1,0,0] op_sel_hi:[1,1,1]
	v_pk_fma_f32 v[126:127], v[84:85], v[28:29], v[126:127] op_sel:[1,0,0] op_sel_hi:[1,1,1]
	v_pk_fma_f32 v[128:129], v[84:85], v[30:31], v[128:129] op_sel:[1,0,0] op_sel_hi:[1,1,1]
	v_pk_fma_f32 v[122:123], v[84:85], v[32:33], v[122:123] op_sel:[1,0,0] op_sel_hi:[1,1,1]
	ds_read_b128 v[26:29], v43 offset:1376
	ds_read_b128 v[30:33], v43 offset:1392
	s_waitcnt vmcnt(23) lgkmcnt(6)
	v_pk_fma_f32 v[124:125], v[86:87], v[2:3], v[124:125] op_sel_hi:[0,1,1]
	v_pk_fma_f32 v[126:127], v[86:87], v[4:5], v[126:127] op_sel_hi:[0,1,1]
	v_pk_fma_f32 v[128:129], v[86:87], v[6:7], v[128:129] op_sel_hi:[0,1,1]
	v_pk_fma_f32 v[122:123], v[86:87], v[8:9], v[122:123] op_sel_hi:[0,1,1]
	ds_read_b128 v[2:5], v43 offset:1408
	ds_read_b128 v[6:9], v43 offset:1424
	s_waitcnt vmcnt(22) lgkmcnt(6)
	v_pk_fma_f32 v[124:125], v[86:87], v[10:11], v[124:125] op_sel:[1,0,0] op_sel_hi:[1,1,1]
	v_pk_fma_f32 v[126:127], v[86:87], v[12:13], v[126:127] op_sel:[1,0,0] op_sel_hi:[1,1,1]
	v_pk_fma_f32 v[128:129], v[86:87], v[14:15], v[128:129] op_sel:[1,0,0] op_sel_hi:[1,1,1]
	v_pk_fma_f32 v[122:123], v[86:87], v[16:17], v[122:123] op_sel:[1,0,0] op_sel_hi:[1,1,1]
	ds_read_b128 v[10:13], v43 offset:1440
	ds_read_b128 v[14:17], v43 offset:1456
	s_waitcnt vmcnt(21) lgkmcnt(6)
	v_pk_fma_f32 v[124:125], v[88:89], v[18:19], v[124:125] op_sel_hi:[0,1,1]
	v_pk_fma_f32 v[126:127], v[88:89], v[20:21], v[126:127] op_sel_hi:[0,1,1]
	v_pk_fma_f32 v[128:129], v[88:89], v[22:23], v[128:129] op_sel_hi:[0,1,1]
	v_pk_fma_f32 v[122:123], v[88:89], v[24:25], v[122:123] op_sel_hi:[0,1,1]
	ds_read_b128 v[18:21], v43 offset:1472
	ds_read_b128 v[22:25], v43 offset:1488
	s_waitcnt vmcnt(20) lgkmcnt(6)
	v_pk_fma_f32 v[124:125], v[88:89], v[26:27], v[124:125] op_sel:[1,0,0] op_sel_hi:[1,1,1]
	v_pk_fma_f32 v[126:127], v[88:89], v[28:29], v[126:127] op_sel:[1,0,0] op_sel_hi:[1,1,1]
	v_pk_fma_f32 v[128:129], v[88:89], v[30:31], v[128:129] op_sel:[1,0,0] op_sel_hi:[1,1,1]
	v_pk_fma_f32 v[122:123], v[88:89], v[32:33], v[122:123] op_sel:[1,0,0] op_sel_hi:[1,1,1]
	ds_read_b128 v[26:29], v43 offset:1504
	ds_read_b128 v[30:33], v43 offset:1520
	s_waitcnt vmcnt(19) lgkmcnt(6)
	v_pk_fma_f32 v[124:125], v[90:91], v[2:3], v[124:125] op_sel_hi:[0,1,1]
	v_pk_fma_f32 v[126:127], v[90:91], v[4:5], v[126:127] op_sel_hi:[0,1,1]
	v_pk_fma_f32 v[128:129], v[90:91], v[6:7], v[128:129] op_sel_hi:[0,1,1]
	v_pk_fma_f32 v[122:123], v[90:91], v[8:9], v[122:123] op_sel_hi:[0,1,1]
	ds_read_b128 v[2:5], v43 offset:1536
	ds_read_b128 v[6:9], v43 offset:1552
	s_waitcnt vmcnt(18) lgkmcnt(6)
	v_pk_fma_f32 v[124:125], v[90:91], v[10:11], v[124:125] op_sel:[1,0,0] op_sel_hi:[1,1,1]
	v_pk_fma_f32 v[126:127], v[90:91], v[12:13], v[126:127] op_sel:[1,0,0] op_sel_hi:[1,1,1]
	v_pk_fma_f32 v[128:129], v[90:91], v[14:15], v[128:129] op_sel:[1,0,0] op_sel_hi:[1,1,1]
	v_pk_fma_f32 v[122:123], v[90:91], v[16:17], v[122:123] op_sel:[1,0,0] op_sel_hi:[1,1,1]
	ds_read_b128 v[10:13], v43 offset:1568
	ds_read_b128 v[14:17], v43 offset:1584
	s_waitcnt vmcnt(17) lgkmcnt(6)
	v_pk_fma_f32 v[124:125], v[92:93], v[18:19], v[124:125] op_sel_hi:[0,1,1]
	v_pk_fma_f32 v[126:127], v[92:93], v[20:21], v[126:127] op_sel_hi:[0,1,1]
	v_pk_fma_f32 v[128:129], v[92:93], v[22:23], v[128:129] op_sel_hi:[0,1,1]
	v_pk_fma_f32 v[122:123], v[92:93], v[24:25], v[122:123] op_sel_hi:[0,1,1]
	ds_read_b128 v[18:21], v43 offset:1600
	ds_read_b128 v[22:25], v43 offset:1616
	s_waitcnt vmcnt(16) lgkmcnt(6)
	v_pk_fma_f32 v[124:125], v[92:93], v[26:27], v[124:125] op_sel:[1,0,0] op_sel_hi:[1,1,1]
	v_pk_fma_f32 v[126:127], v[92:93], v[28:29], v[126:127] op_sel:[1,0,0] op_sel_hi:[1,1,1]
	v_pk_fma_f32 v[128:129], v[92:93], v[30:31], v[128:129] op_sel:[1,0,0] op_sel_hi:[1,1,1]
	v_pk_fma_f32 v[122:123], v[92:93], v[32:33], v[122:123] op_sel:[1,0,0] op_sel_hi:[1,1,1]
	ds_read_b128 v[26:29], v43 offset:1632
	ds_read_b128 v[30:33], v43 offset:1648
	s_waitcnt vmcnt(15) lgkmcnt(6)
	v_pk_fma_f32 v[124:125], v[94:95], v[2:3], v[124:125] op_sel_hi:[0,1,1]
	v_pk_fma_f32 v[126:127], v[94:95], v[4:5], v[126:127] op_sel_hi:[0,1,1]
	v_pk_fma_f32 v[128:129], v[94:95], v[6:7], v[128:129] op_sel_hi:[0,1,1]
	v_pk_fma_f32 v[122:123], v[94:95], v[8:9], v[122:123] op_sel_hi:[0,1,1]
	ds_read_b128 v[2:5], v43 offset:1664
	ds_read_b128 v[6:9], v43 offset:1680
	s_waitcnt vmcnt(14) lgkmcnt(6)
	v_pk_fma_f32 v[124:125], v[94:95], v[10:11], v[124:125] op_sel:[1,0,0] op_sel_hi:[1,1,1]
	v_pk_fma_f32 v[126:127], v[94:95], v[12:13], v[126:127] op_sel:[1,0,0] op_sel_hi:[1,1,1]
	v_pk_fma_f32 v[128:129], v[94:95], v[14:15], v[128:129] op_sel:[1,0,0] op_sel_hi:[1,1,1]
	v_pk_fma_f32 v[122:123], v[94:95], v[16:17], v[122:123] op_sel:[1,0,0] op_sel_hi:[1,1,1]
	ds_read_b128 v[10:13], v43 offset:1696
	ds_read_b128 v[14:17], v43 offset:1712
	s_waitcnt vmcnt(13) lgkmcnt(6)
	v_pk_fma_f32 v[124:125], v[96:97], v[18:19], v[124:125] op_sel_hi:[0,1,1]
	v_pk_fma_f32 v[126:127], v[96:97], v[20:21], v[126:127] op_sel_hi:[0,1,1]
	v_pk_fma_f32 v[128:129], v[96:97], v[22:23], v[128:129] op_sel_hi:[0,1,1]
	v_pk_fma_f32 v[122:123], v[96:97], v[24:25], v[122:123] op_sel_hi:[0,1,1]
	ds_read_b128 v[18:21], v43 offset:1728
	ds_read_b128 v[22:25], v43 offset:1744
	s_waitcnt vmcnt(12) lgkmcnt(6)
	v_pk_fma_f32 v[124:125], v[96:97], v[26:27], v[124:125] op_sel:[1,0,0] op_sel_hi:[1,1,1]
	v_pk_fma_f32 v[126:127], v[96:97], v[28:29], v[126:127] op_sel:[1,0,0] op_sel_hi:[1,1,1]
	v_pk_fma_f32 v[128:129], v[96:97], v[30:31], v[128:129] op_sel:[1,0,0] op_sel_hi:[1,1,1]
	v_pk_fma_f32 v[122:123], v[96:97], v[32:33], v[122:123] op_sel:[1,0,0] op_sel_hi:[1,1,1]
	ds_read_b128 v[26:29], v43 offset:1760
	ds_read_b128 v[30:33], v43 offset:1776
	s_waitcnt vmcnt(11) lgkmcnt(6)
; #define LAS __attribute__((address_space(3)))
; __device__ __forceinline__ void ph0_adaln(const Args& a, LAS unsigned char* lds, int tid, int G, int bid) {
;     ...
;         for (int k = 0; k < 256; k += 64) {
;             float w[64];
; #pragma unroll
;             for (int q = 0; q < 64; ++q) w[q] = wp[(size_t)(k + q) * MODW];
; #pragma unroll
;             for (int q = 0; q < 64; ++q) { const f32x4 c0 = *(const LAS f32x4*)(cond + (kq * 256 + k + q) * 8), c1 = *(const LAS f32x4*)(cond + (kq * 256 + k + q) * 8 + 4);
;                 acc[0] += w[q] * c0[0]; acc[1] += w[q] * c0[1]; acc[2] += w[q] * c0[2]; acc[3] += w[q] * c0[3];
;                 acc[4] += w[q] * c1[0]; acc[5] += w[q] * c1[1]; acc[6] += w[q] * c1[2]; acc[7] += w[q] * c1[3]; }
;         }
; #pragma unroll
;         for (int b = 0; b < 8; ++b) red[(kq * 8 + b) * 64 + cc] = acc[b];
;         __syncthreads();
;         { const int b = tid >> 6;
;           float s = 0.f;
; #pragma unroll
;           for (int q = 0; q < 8; ++q) s += red[(q * 8 + b) * 64 + cc];
;           MOD[(size_t)b * MODW + col] = s + bada[col]; }
;         __syncthreads();
	v_pk_fma_f32 v[124:125], v[98:99], v[2:3], v[124:125] op_sel_hi:[0,1,1]
	v_pk_fma_f32 v[126:127], v[98:99], v[4:5], v[126:127] op_sel_hi:[0,1,1]
	v_pk_fma_f32 v[128:129], v[98:99], v[6:7], v[128:129] op_sel_hi:[0,1,1]
	v_pk_fma_f32 v[122:123], v[98:99], v[8:9], v[122:123] op_sel_hi:[0,1,1]
	ds_read_b128 v[2:5], v43 offset:1792
	ds_read_b128 v[6:9], v43 offset:1808
	s_waitcnt vmcnt(10) lgkmcnt(6)
	v_pk_fma_f32 v[124:125], v[98:99], v[10:11], v[124:125] op_sel:[1,0,0] op_sel_hi:[1,1,1]
	v_pk_fma_f32 v[126:127], v[98:99], v[12:13], v[126:127] op_sel:[1,0,0] op_sel_hi:[1,1,1]
	v_pk_fma_f32 v[128:129], v[98:99], v[14:15], v[128:129] op_sel:[1,0,0] op_sel_hi:[1,1,1]
	v_pk_fma_f32 v[122:123], v[98:99], v[16:17], v[122:123] op_sel:[1,0,0] op_sel_hi:[1,1,1]
	ds_read_b128 v[10:13], v43 offset:1824
	ds_read_b128 v[14:17], v43 offset:1840
	s_waitcnt vmcnt(9) lgkmcnt(6)
	v_pk_fma_f32 v[124:125], v[100:101], v[18:19], v[124:125] op_sel_hi:[0,1,1]
	v_pk_fma_f32 v[126:127], v[100:101], v[20:21], v[126:127] op_sel_hi:[0,1,1]
	v_pk_fma_f32 v[128:129], v[100:101], v[22:23], v[128:129] op_sel_hi:[0,1,1]
	v_pk_fma_f32 v[122:123], v[100:101], v[24:25], v[122:123] op_sel_hi:[0,1,1]
	ds_read_b128 v[18:21], v43 offset:1856
	ds_read_b128 v[22:25], v43 offset:1872
	s_waitcnt vmcnt(8) lgkmcnt(6)
	v_pk_fma_f32 v[124:125], v[100:101], v[26:27], v[124:125] op_sel:[1,0,0] op_sel_hi:[1,1,1]
	v_pk_fma_f32 v[126:127], v[100:101], v[28:29], v[126:127] op_sel:[1,0,0] op_sel_hi:[1,1,1]
	v_pk_fma_f32 v[128:129], v[100:101], v[30:31], v[128:129] op_sel:[1,0,0] op_sel_hi:[1,1,1]
	v_pk_fma_f32 v[122:123], v[100:101], v[32:33], v[122:123] op_sel:[1,0,0] op_sel_hi:[1,1,1]
	ds_read_b128 v[26:29], v43 offset:1888
	ds_read_b128 v[30:33], v43 offset:1904
	s_waitcnt vmcnt(7) lgkmcnt(6)
	v_pk_fma_f32 v[124:125], v[102:103], v[2:3], v[124:125] op_sel_hi:[0,1,1]
	v_pk_fma_f32 v[126:127], v[102:103], v[4:5], v[126:127] op_sel_hi:[0,1,1]
	v_pk_fma_f32 v[128:129], v[102:103], v[6:7], v[128:129] op_sel_hi:[0,1,1]
	v_pk_fma_f32 v[122:123], v[102:103], v[8:9], v[122:123] op_sel_hi:[0,1,1]
	ds_read_b128 v[2:5], v43 offset:1920
	ds_read_b128 v[6:9], v43 offset:1936
	s_waitcnt vmcnt(6) lgkmcnt(6)
	v_pk_fma_f32 v[124:125], v[102:103], v[10:11], v[124:125] op_sel:[1,0,0] op_sel_hi:[1,1,1]
	v_pk_fma_f32 v[126:127], v[102:103], v[12:13], v[126:127] op_sel:[1,0,0] op_sel_hi:[1,1,1]
	v_pk_fma_f32 v[128:129], v[102:103], v[14:15], v[128:129] op_sel:[1,0,0] op_sel_hi:[1,1,1]
	v_pk_fma_f32 v[122:123], v[102:103], v[16:17], v[122:123] op_sel:[1,0,0] op_sel_hi:[1,1,1]
	ds_read_b128 v[10:13], v43 offset:1952
	ds_read_b128 v[14:17], v43 offset:1968
	s_waitcnt vmcnt(5) lgkmcnt(6)
	v_pk_fma_f32 v[124:125], v[104:105], v[18:19], v[124:125] op_sel_hi:[0,1,1]
	v_pk_fma_f32 v[126:127], v[104:105], v[20:21], v[126:127] op_sel_hi:[0,1,1]
	v_pk_fma_f32 v[128:129], v[104:105], v[22:23], v[128:129] op_sel_hi:[0,1,1]
	v_pk_fma_f32 v[122:123], v[104:105], v[24:25], v[122:123] op_sel_hi:[0,1,1]
	ds_read_b128 v[18:21], v43 offset:1984
	ds_read_b128 v[22:25], v43 offset:2000
	s_waitcnt vmcnt(4) lgkmcnt(6)
	v_pk_fma_f32 v[124:125], v[104:105], v[26:27], v[124:125] op_sel:[1,0,0] op_sel_hi:[1,1,1]
	v_pk_fma_f32 v[126:127], v[104:105], v[28:29], v[126:127] op_sel:[1,0,0] op_sel_hi:[1,1,1]
	v_pk_fma_f32 v[128:129], v[104:105], v[30:31], v[128:129] op_sel:[1,0,0] op_sel_hi:[1,1,1]
	v_pk_fma_f32 v[122:123], v[104:105], v[32:33], v[122:123] op_sel:[1,0,0] op_sel_hi:[1,1,1]
	ds_read_b128 v[26:29], v43 offset:2016
	ds_read_b128 v[30:33], v43 offset:2032
	s_waitcnt vmcnt(3) lgkmcnt(6)
	v_pk_fma_f32 v[124:125], v[106:107], v[2:3], v[124:125] op_sel_hi:[0,1,1]
	v_pk_fma_f32 v[126:127], v[106:107], v[4:5], v[126:127] op_sel_hi:[0,1,1]
	v_pk_fma_f32 v[128:129], v[106:107], v[6:7], v[128:129] op_sel_hi:[0,1,1]
	v_pk_fma_f32 v[122:123], v[106:107], v[8:9], v[122:123] op_sel_hi:[0,1,1]
	s_waitcnt vmcnt(2) lgkmcnt(4)
	v_pk_fma_f32 v[124:125], v[106:107], v[10:11], v[124:125] op_sel:[1,0,0] op_sel_hi:[1,1,1]
	v_pk_fma_f32 v[126:127], v[106:107], v[12:13], v[126:127] op_sel:[1,0,0] op_sel_hi:[1,1,1]
	v_pk_fma_f32 v[128:129], v[106:107], v[14:15], v[128:129] op_sel:[1,0,0] op_sel_hi:[1,1,1]
	v_pk_fma_f32 v[122:123], v[106:107], v[16:17], v[122:123] op_sel:[1,0,0] op_sel_hi:[1,1,1]
	s_waitcnt vmcnt(1) lgkmcnt(2)
	v_pk_fma_f32 v[124:125], v[108:109], v[18:19], v[124:125] op_sel_hi:[0,1,1]
	v_pk_fma_f32 v[126:127], v[108:109], v[20:21], v[126:127] op_sel_hi:[0,1,1]
	v_pk_fma_f32 v[128:129], v[108:109], v[22:23], v[128:129] op_sel_hi:[0,1,1]
	v_pk_fma_f32 v[122:123], v[108:109], v[24:25], v[122:123] op_sel_hi:[0,1,1]
	s_waitcnt vmcnt(0) lgkmcnt(0)
	v_pk_fma_f32 v[124:125], v[108:109], v[26:27], v[124:125] op_sel:[1,0,0] op_sel_hi:[1,1,1]
	v_pk_fma_f32 v[126:127], v[108:109], v[28:29], v[126:127] op_sel:[1,0,0] op_sel_hi:[1,1,1]
	v_pk_fma_f32 v[128:129], v[108:109], v[30:31], v[128:129] op_sel:[1,0,0] op_sel_hi:[1,1,1]
	v_pk_fma_f32 v[122:123], v[108:109], v[32:33], v[122:123] op_sel:[1,0,0] op_sel_hi:[1,1,1]
	v_readlane_b32 s34, v250, 58
	v_readlane_b32 s35, v250, 59
	s_load_dwordx16 s[4:19], s[34:35], 0x0
	v_readlane_b32 s20, v250, 60
	ds_write2st64_b32 v151, v124, v125 offset1:1
	ds_write2st64_b32 v151, v126, v127 offset0:2 offset1:3
	ds_write2st64_b32 v151, v128, v129 offset0:4 offset1:5
	ds_write2st64_b32 v151, v122, v123 offset0:6 offset1:7
	v_lshl_or_b32 v2, s20, 6, v178
	v_ashrrev_i32_e32 v3, 31, v2
	v_lshlrev_b64 v[2:3], 2, v[2:3]
	s_waitcnt lgkmcnt(0)
	v_lshl_add_u64 v[4:5], s[10:11], 0, v[2:3]
	s_barrier
	global_load_dword v12, v[4:5], off
	ds_read2st64_b32 v[4:5], v147 offset1:8
	ds_read2st64_b32 v[6:7], v147 offset0:16 offset1:24
	ds_read2st64_b32 v[8:9], v147 offset0:32 offset1:40
	ds_read2st64_b32 v[10:11], v147 offset0:48 offset1:56
	s_load_dword s88, s[34:35], 0xf8
	s_load_dwordx4 s[80:83], s[34:35], 0xe0
	s_waitcnt lgkmcnt(0)
	v_add_f32_e32 v4, 0, v4
	v_add_f32_e32 v4, v4, v5
	v_add_f32_e32 v4, v4, v6
	v_add_f32_e32 v4, v4, v7
	v_add_f32_e32 v4, v4, v8
	v_add_f32_e32 v4, v4, v9
	v_add_f32_e32 v4, v4, v10
	s_add_i32 s20, s20, s88
	v_readlane_b32 s0, v250, 57
	v_add_f32_e32 v4, v4, v11
	s_cmpk_gt_i32 s20, 0xbf
	v_add_u32_e32 v42, s0, v42
	v_lshl_add_u64 v[2:3], v[36:37], 0, v[2:3]
	s_mov_b64 s[2:3], -1
	v_readlane_b32 s84, v250, 50
	s_waitcnt vmcnt(0)
	v_add_f32_e32 v4, v4, v12
	global_store_dword v[2:3], v4, off
	s_barrier
	s_cbranch_scc0 .LBB0_23
